# speedup vs baseline: 1.0073x; 1.0073x over previous
.LBB6_12:
	ds_read_b128 v[176:179], v169
	ds_read_b128 v[180:183], v170
	ds_read_b128 v[184:187], v171
	ds_read_b128 v[188:191], v172
	v_add_u32_e32 v174, 0xc000, v152
	v_lshl_add_u64 v[192:193], v[136:137], 0, s[44:45]
	v_add_u32_e32 v175, 0xe000, v152
	v_add_u32_e32 v173, s17, v168
	v_lshl_add_u64 v[232:233], v[192:193], 0, s[30:31]
	s_mov_b32 m0, s72
	v_lshl_add_u64 v[248:249], v[134:135], 0, s[44:45]
	ds_read_b128 v[196:199], v173
	ds_read_b128 v[200:203], v173 offset:1024
	ds_read_b128 v[204:207], v173 offset:2048
	ds_read_b128 v[212:215], v173 offset:3072
	ds_read_b128 v[216:219], v173 offset:4096
	ds_read_b128 v[220:223], v173 offset:5120
	ds_read_b128 v[224:227], v173 offset:6144
	ds_read_b128 v[228:231], v173 offset:7168
	global_load_lds_dwordx4 v[232:233], off
	s_mov_b32 m0, s73
	v_lshl_add_u64 v[232:233], v[248:249], 0, s[30:31]
	global_load_lds_dwordx4 v[232:233], off
	s_waitcnt lgkmcnt(8)
	s_barrier
	s_waitcnt lgkmcnt(0)
	v_mfma_f32_16x16x32_f16 v[2:5], v[196:199], v[176:179], v[2:5]
	v_mfma_f32_16x16x32_f16 v[6:9], v[196:199], v[184:187], v[6:9]
	v_mfma_f32_16x16x32_f16 v[10:13], v[204:207], v[176:179], v[10:13]
	v_mfma_f32_16x16x32_f16 v[18:21], v[204:207], v[184:187], v[18:21]
	v_mfma_f32_16x16x32_f16 v[30:33], v[216:219], v[176:179], v[30:33]
	v_mfma_f32_16x16x32_f16 v[42:45], v[216:219], v[184:187], v[42:45]
	v_mfma_f32_16x16x32_f16 v[54:57], v[224:227], v[176:179], v[54:57]
	v_mfma_f32_16x16x32_f16 v[66:69], v[224:227], v[184:187], v[66:69]
	v_mfma_f32_16x16x32_f16 v[2:5], v[200:203], v[180:183], v[2:5]
	v_mfma_f32_16x16x32_f16 v[6:9], v[200:203], v[188:191], v[6:9]
	v_mfma_f32_16x16x32_f16 v[10:13], v[212:215], v[180:183], v[10:13]
	v_mfma_f32_16x16x32_f16 v[18:21], v[212:215], v[188:191], v[18:21]
	v_mfma_f32_16x16x32_f16 v[30:33], v[220:223], v[180:183], v[30:33]
	v_mfma_f32_16x16x32_f16 v[42:45], v[220:223], v[188:191], v[42:45]
	v_mfma_f32_16x16x32_f16 v[54:57], v[228:231], v[180:183], v[54:57]
	v_mfma_f32_16x16x32_f16 v[66:69], v[228:231], v[188:191], v[66:69]
	s_barrier
	v_lshl_add_u64 v[250:251], v[140:141], 0, s[44:45]
	v_lshl_add_u64 v[252:253], v[250:251], 0, s[34:35]
	s_mov_b32 m0, s74
	ds_read_b128 v[232:235], v161
	ds_read_b128 v[236:239], v162
	ds_read_b128 v[240:243], v163
	ds_read_b128 v[244:247], v164
	global_load_lds_dwordx4 v[252:253], off
	v_lshl_add_u64 v[252:253], v[138:139], 0, s[44:45]
	s_mov_b32 m0, s75
	v_lshl_add_u64 v[254:255], v[252:253], 0, s[34:35]
	global_load_lds_dwordx4 v[254:255], off
	s_barrier
	s_waitcnt lgkmcnt(0)
	v_mfma_f32_16x16x32_f16 v[14:17], v[196:199], v[232:235], v[14:17]
	v_mfma_f32_16x16x32_f16 v[22:25], v[196:199], v[240:243], v[22:25]
	v_mfma_f32_16x16x32_f16 v[34:37], v[204:207], v[232:235], v[34:37]
	v_mfma_f32_16x16x32_f16 v[46:49], v[204:207], v[240:243], v[46:49]
	v_mfma_f32_16x16x32_f16 v[58:61], v[216:219], v[232:235], v[58:61]
	v_mfma_f32_16x16x32_f16 v[70:73], v[216:219], v[240:243], v[70:73]
	v_mfma_f32_16x16x32_f16 v[78:81], v[224:227], v[232:235], v[78:81]
	v_mfma_f32_16x16x32_f16 v[86:89], v[224:227], v[240:243], v[86:89]
	v_mfma_f32_16x16x32_f16 v[14:17], v[200:203], v[236:239], v[14:17]
	v_mfma_f32_16x16x32_f16 v[22:25], v[200:203], v[244:247], v[22:25]
	v_mfma_f32_16x16x32_f16 v[34:37], v[212:215], v[236:239], v[34:37]
	v_mfma_f32_16x16x32_f16 v[46:49], v[212:215], v[244:247], v[46:49]
	v_mfma_f32_16x16x32_f16 v[58:61], v[220:223], v[236:239], v[58:61]
	v_mfma_f32_16x16x32_f16 v[70:73], v[220:223], v[244:247], v[70:73]
	v_mfma_f32_16x16x32_f16 v[78:81], v[228:231], v[236:239], v[78:81]
	v_mfma_f32_16x16x32_f16 v[86:89], v[228:231], v[244:247], v[86:89]
	v_lshl_add_u64 v[254:255], v[192:193], 0, s[34:35]
	s_mov_b32 m0, s76
	s_barrier
	ds_read_b128 v[196:199], v173 offset:16384
	ds_read_b128 v[200:203], v173 offset:17408
	ds_read_b128 v[204:207], v173 offset:18432
	ds_read_b128 v[212:215], v173 offset:19456
	ds_read_b128 v[216:219], v173 offset:20480
	ds_read_b128 v[220:223], v173 offset:21504
	ds_read_b128 v[224:227], v173 offset:22528
	ds_read_b128 v[228:231], v173 offset:23552
	global_load_lds_dwordx4 v[254:255], off
	s_mov_b32 m0, s77
	v_lshl_add_u64 v[254:255], v[248:249], 0, s[34:35]
	global_load_lds_dwordx4 v[254:255], off
	s_barrier
	s_waitcnt lgkmcnt(0)
	v_mfma_f32_16x16x32_f16 v[26:29], v[196:199], v[176:179], v[26:29]
	v_mfma_f32_16x16x32_f16 v[38:41], v[196:199], v[184:187], v[38:41]
	v_mfma_f32_16x16x32_f16 v[50:53], v[204:207], v[176:179], v[50:53]
	v_mfma_f32_16x16x32_f16 v[62:65], v[204:207], v[184:187], v[62:65]
	v_mfma_f32_16x16x32_f16 v[74:77], v[216:219], v[176:179], v[74:77]
	v_mfma_f32_16x16x32_f16 v[82:85], v[216:219], v[184:187], v[82:85]
	v_mfma_f32_16x16x32_f16 v[90:93], v[224:227], v[176:179], v[90:93]
	v_mfma_f32_16x16x32_f16 v[94:97], v[224:227], v[184:187], v[94:97]
	v_mfma_f32_16x16x32_f16 v[26:29], v[200:203], v[180:183], v[26:29]
	v_mfma_f32_16x16x32_f16 v[38:41], v[200:203], v[188:191], v[38:41]
	v_mfma_f32_16x16x32_f16 v[50:53], v[212:215], v[180:183], v[50:53]
	v_mfma_f32_16x16x32_f16 v[62:65], v[212:215], v[188:191], v[62:65]
	v_mfma_f32_16x16x32_f16 v[74:77], v[220:223], v[180:183], v[74:77]
	v_mfma_f32_16x16x32_f16 v[82:85], v[220:223], v[188:191], v[82:85]
	v_mfma_f32_16x16x32_f16 v[90:93], v[228:231], v[180:183], v[90:93]
	v_mfma_f32_16x16x32_f16 v[94:97], v[228:231], v[188:191], v[94:97]
	s_barrier
	s_mov_b32 m0, s78
	v_lshl_add_u64 v[176:177], v[250:251], 0, s[36:37]
	global_load_lds_dwordx4 v[176:177], off
	s_mov_b32 m0, s79
	v_lshl_add_u64 v[176:177], v[252:253], 0, s[36:37]
	global_load_lds_dwordx4 v[176:177], off
	s_waitcnt vmcnt(6)
	s_barrier
	v_mfma_f32_16x16x32_f16 v[98:101], v[196:199], v[232:235], v[98:101]
	v_mfma_f32_16x16x32_f16 v[102:105], v[196:199], v[240:243], v[102:105]
	v_mfma_f32_16x16x32_f16 v[106:109], v[204:207], v[232:235], v[106:109]
	v_mfma_f32_16x16x32_f16 v[110:113], v[204:207], v[240:243], v[110:113]
	v_mfma_f32_16x16x32_f16 v[114:117], v[216:219], v[232:235], v[114:117]
	v_mfma_f32_16x16x32_f16 v[118:121], v[216:219], v[240:243], v[118:121]
	v_mfma_f32_16x16x32_f16 v[122:125], v[224:227], v[232:235], v[122:125]
	v_mfma_f32_16x16x32_f16 v[126:129], v[224:227], v[240:243], v[126:129]
	v_mfma_f32_16x16x32_f16 v[98:101], v[200:203], v[236:239], v[98:101]
	v_mfma_f32_16x16x32_f16 v[102:105], v[200:203], v[244:247], v[102:105]
	v_mfma_f32_16x16x32_f16 v[106:109], v[212:215], v[236:239], v[106:109]
	v_mfma_f32_16x16x32_f16 v[110:113], v[212:215], v[244:247], v[110:113]
	v_mfma_f32_16x16x32_f16 v[114:117], v[220:223], v[236:239], v[114:117]
	v_mfma_f32_16x16x32_f16 v[118:121], v[220:223], v[244:247], v[118:121]
	v_mfma_f32_16x16x32_f16 v[122:125], v[228:231], v[236:239], v[122:125]
	v_mfma_f32_16x16x32_f16 v[126:129], v[228:231], v[244:247], v[126:129]
	s_barrier
	ds_read_b128 v[176:179], v148
	ds_read_b128 v[180:183], v149
	ds_read_b128 v[184:187], v150
	ds_read_b128 v[188:191], v151
	v_lshl_add_u64 v[232:233], v[192:193], 0, s[36:37]
	s_mov_b32 m0, s80
	ds_read_b128 v[196:199], v173 offset:32768
	ds_read_b128 v[200:203], v173 offset:33792
	ds_read_b128 v[204:207], v173 offset:34816
	ds_read_b128 v[212:215], v173 offset:35840
	ds_read_b128 v[216:219], v173 offset:36864
	ds_read_b128 v[220:223], v173 offset:37888
	ds_read_b128 v[224:227], v173 offset:38912
	ds_read_b128 v[228:231], v173 offset:39936
	global_load_lds_dwordx4 v[232:233], off
	s_mov_b32 m0, s81
	v_lshl_add_u64 v[232:233], v[248:249], 0, s[36:37]
	global_load_lds_dwordx4 v[232:233], off
	s_waitcnt lgkmcnt(8)
	s_barrier
	s_waitcnt lgkmcnt(0)
	v_mfma_f32_16x16x32_f16 v[2:5], v[196:199], v[176:179], v[2:5]
	v_mfma_f32_16x16x32_f16 v[6:9], v[196:199], v[184:187], v[6:9]
	v_mfma_f32_16x16x32_f16 v[10:13], v[204:207], v[176:179], v[10:13]
	v_mfma_f32_16x16x32_f16 v[18:21], v[204:207], v[184:187], v[18:21]
	v_mfma_f32_16x16x32_f16 v[30:33], v[216:219], v[176:179], v[30:33]
	v_mfma_f32_16x16x32_f16 v[42:45], v[216:219], v[184:187], v[42:45]
	v_mfma_f32_16x16x32_f16 v[54:57], v[224:227], v[176:179], v[54:57]
	v_mfma_f32_16x16x32_f16 v[66:69], v[224:227], v[184:187], v[66:69]
	v_mfma_f32_16x16x32_f16 v[2:5], v[200:203], v[180:183], v[2:5]
	v_mfma_f32_16x16x32_f16 v[6:9], v[200:203], v[188:191], v[6:9]
	v_mfma_f32_16x16x32_f16 v[10:13], v[212:215], v[180:183], v[10:13]
	v_mfma_f32_16x16x32_f16 v[18:21], v[212:215], v[188:191], v[18:21]
	v_mfma_f32_16x16x32_f16 v[30:33], v[220:223], v[180:183], v[30:33]
	v_mfma_f32_16x16x32_f16 v[42:45], v[220:223], v[188:191], v[42:45]
	v_mfma_f32_16x16x32_f16 v[54:57], v[228:231], v[180:183], v[54:57]
	v_mfma_f32_16x16x32_f16 v[66:69], v[228:231], v[188:191], v[66:69]
	s_barrier
	v_lshl_add_u64 v[254:255], v[250:251], 0, s[38:39]
	s_mov_b32 m0, s82
	ds_read_b128 v[232:235], v142
	ds_read_b128 v[236:239], v143
	ds_read_b128 v[240:243], v144
	ds_read_b128 v[244:247], v145
	global_load_lds_dwordx4 v[254:255], off
	s_mov_b32 m0, s83
	v_lshl_add_u64 v[254:255], v[252:253], 0, s[38:39]
	global_load_lds_dwordx4 v[254:255], off
	s_barrier
	s_waitcnt lgkmcnt(0)
	v_mfma_f32_16x16x32_f16 v[14:17], v[196:199], v[232:235], v[14:17]
	v_mfma_f32_16x16x32_f16 v[22:25], v[196:199], v[240:243], v[22:25]
	v_mfma_f32_16x16x32_f16 v[34:37], v[204:207], v[232:235], v[34:37]
	v_mfma_f32_16x16x32_f16 v[46:49], v[204:207], v[240:243], v[46:49]
	v_mfma_f32_16x16x32_f16 v[58:61], v[216:219], v[232:235], v[58:61]
	v_mfma_f32_16x16x32_f16 v[70:73], v[216:219], v[240:243], v[70:73]
	v_mfma_f32_16x16x32_f16 v[78:81], v[224:227], v[232:235], v[78:81]
	v_mfma_f32_16x16x32_f16 v[86:89], v[224:227], v[240:243], v[86:89]
	v_mfma_f32_16x16x32_f16 v[14:17], v[200:203], v[236:239], v[14:17]
	v_mfma_f32_16x16x32_f16 v[22:25], v[200:203], v[244:247], v[22:25]
	v_mfma_f32_16x16x32_f16 v[34:37], v[212:215], v[236:239], v[34:37]
	v_mfma_f32_16x16x32_f16 v[46:49], v[212:215], v[244:247], v[46:49]
	v_mfma_f32_16x16x32_f16 v[58:61], v[220:223], v[236:239], v[58:61]
	v_mfma_f32_16x16x32_f16 v[70:73], v[220:223], v[244:247], v[70:73]
	v_mfma_f32_16x16x32_f16 v[78:81], v[228:231], v[236:239], v[78:81]
	v_mfma_f32_16x16x32_f16 v[86:89], v[228:231], v[244:247], v[86:89]
	v_lshl_add_u64 v[192:193], v[192:193], 0, s[38:39]
	s_mov_b32 m0, s84
	s_barrier
	ds_read_b128 v[196:199], v173 offset:49152
	ds_read_b128 v[200:203], v173 offset:50176
	ds_read_b128 v[204:207], v173 offset:51200
	ds_read_b128 v[212:215], v173 offset:52224
	ds_read_b128 v[216:219], v173 offset:53248
	ds_read_b128 v[220:223], v173 offset:54272
	ds_read_b128 v[224:227], v173 offset:55296
	ds_read_b128 v[228:231], v173 offset:56320
	global_load_lds_dwordx4 v[192:193], off
	s_mov_b32 m0, s85
	v_lshl_add_u64 v[192:193], v[248:249], 0, s[38:39]
	global_load_lds_dwordx4 v[192:193], off
	s_barrier
	s_waitcnt lgkmcnt(0)
	v_mfma_f32_16x16x32_f16 v[26:29], v[196:199], v[176:179], v[26:29]
	v_mfma_f32_16x16x32_f16 v[38:41], v[196:199], v[184:187], v[38:41]
	v_mfma_f32_16x16x32_f16 v[50:53], v[204:207], v[176:179], v[50:53]
	v_mfma_f32_16x16x32_f16 v[62:65], v[204:207], v[184:187], v[62:65]
	v_mfma_f32_16x16x32_f16 v[74:77], v[216:219], v[176:179], v[74:77]
	v_mfma_f32_16x16x32_f16 v[82:85], v[216:219], v[184:187], v[82:85]
	v_mfma_f32_16x16x32_f16 v[90:93], v[224:227], v[176:179], v[90:93]
	v_mfma_f32_16x16x32_f16 v[94:97], v[224:227], v[184:187], v[94:97]
	v_mfma_f32_16x16x32_f16 v[26:29], v[200:203], v[180:183], v[26:29]
	v_mfma_f32_16x16x32_f16 v[38:41], v[200:203], v[188:191], v[38:41]
	v_mfma_f32_16x16x32_f16 v[50:53], v[212:215], v[180:183], v[50:53]
	v_mfma_f32_16x16x32_f16 v[62:65], v[212:215], v[188:191], v[62:65]
	v_mfma_f32_16x16x32_f16 v[74:77], v[220:223], v[180:183], v[74:77]
	v_mfma_f32_16x16x32_f16 v[82:85], v[220:223], v[188:191], v[82:85]
	v_mfma_f32_16x16x32_f16 v[90:93], v[228:231], v[180:183], v[90:93]
	v_mfma_f32_16x16x32_f16 v[94:97], v[228:231], v[188:191], v[94:97]
	s_barrier
	s_mov_b32 m0, s86
	v_lshl_add_u64 v[176:177], v[250:251], 0, s[40:41]
	global_load_lds_dwordx4 v[176:177], off
	s_mov_b32 m0, s87
	v_lshl_add_u64 v[176:177], v[252:253], 0, s[40:41]
	global_load_lds_dwordx4 v[176:177], off
	s_waitcnt vmcnt(6)
	s_barrier
	v_mfma_f32_16x16x32_f16 v[98:101], v[196:199], v[232:235], v[98:101]
	v_mfma_f32_16x16x32_f16 v[102:105], v[196:199], v[240:243], v[102:105]
	v_mfma_f32_16x16x32_f16 v[106:109], v[204:207], v[232:235], v[106:109]
	v_mfma_f32_16x16x32_f16 v[110:113], v[204:207], v[240:243], v[110:113]
	v_mfma_f32_16x16x32_f16 v[114:117], v[216:219], v[232:235], v[114:117]
	v_mfma_f32_16x16x32_f16 v[118:121], v[216:219], v[240:243], v[118:121]
	v_mfma_f32_16x16x32_f16 v[122:125], v[224:227], v[232:235], v[122:125]
	v_mfma_f32_16x16x32_f16 v[126:129], v[224:227], v[240:243], v[126:129]
	v_mfma_f32_16x16x32_f16 v[98:101], v[200:203], v[236:239], v[98:101]
	v_mfma_f32_16x16x32_f16 v[102:105], v[200:203], v[244:247], v[102:105]
	v_mfma_f32_16x16x32_f16 v[106:109], v[212:215], v[236:239], v[106:109]
	v_mfma_f32_16x16x32_f16 v[110:113], v[212:215], v[244:247], v[110:113]
	v_mfma_f32_16x16x32_f16 v[114:117], v[220:223], v[236:239], v[114:117]
	v_mfma_f32_16x16x32_f16 v[118:121], v[220:223], v[244:247], v[118:121]
	v_mfma_f32_16x16x32_f16 v[122:125], v[228:231], v[236:239], v[122:125]
	v_mfma_f32_16x16x32_f16 v[126:129], v[228:231], v[244:247], v[126:129]
	s_add_i32 s46, s46, 2
	s_add_u32 s44, s44, 0x100
	s_addc_u32 s45, s45, 0
	s_cmp_lt_u32 s46, 4
	s_barrier
	s_cbranch_scc1 .LBB6_12
	s_add_u32 s0, s0, 0x20380
	s_addc_u32 s1, s1, 0
	v_readfirstlane_b32 s17, v174
	v_lshl_add_u64 v[130:131], v[130:131], 1, s[0:1]
	s_mov_b32 m0, s17
	ds_read_b128 v[134:137], v169
	ds_read_b128 v[138:141], v170
	ds_read_b128 v[152:155], v171
	ds_read_b128 v[156:159], v172
	ds_read_b128 v[166:169], v173
	ds_read_b128 v[176:179], v173 offset:1024
	ds_read_b128 v[180:183], v173 offset:2048
	ds_read_b128 v[184:187], v173 offset:3072
	ds_read_b128 v[188:191], v173 offset:4096
	ds_read_b128 v[196:199], v173 offset:5120
	ds_read_b128 v[200:203], v173 offset:6144
	ds_read_b128 v[204:207], v173 offset:7168
	global_load_lds_dwordx4 v[130:131], off
	v_lshl_add_u64 v[130:131], v[132:133], 1, s[0:1]
	v_readfirstlane_b32 s0, v175
	s_mov_b32 m0, s0
	s_nop 0
	global_load_lds_dwordx4 v[130:131], off
	s_barrier
	s_waitcnt lgkmcnt(0)
	v_mfma_f32_16x16x32_f16 v[2:5], v[166:169], v[134:137], v[2:5]
	v_mfma_f32_16x16x32_f16 v[42:45], v[188:191], v[152:155], v[42:45]
	v_mfma_f32_16x16x32_f16 v[54:57], v[200:203], v[134:137], v[54:57]
	v_mfma_f32_16x16x32_f16 v[66:69], v[200:203], v[152:155], v[66:69]
	v_mfma_f32_16x16x32_f16 v[2:5], v[176:179], v[138:141], v[2:5]
	v_mfma_f32_16x16x32_f16 v[6:9], v[166:169], v[152:155], v[6:9]
	v_mfma_f32_16x16x32_f16 v[10:13], v[180:183], v[134:137], v[10:13]
	v_mfma_f32_16x16x32_f16 v[18:21], v[180:183], v[152:155], v[18:21]
	v_mfma_f32_16x16x32_f16 v[30:33], v[188:191], v[134:137], v[30:33]
	v_mfma_f32_16x16x32_f16 v[42:45], v[196:199], v[156:159], v[42:45]
	v_mfma_f32_16x16x32_f16 v[54:57], v[204:207], v[138:141], v[54:57]
	v_mfma_f32_16x16x32_f16 v[66:69], v[204:207], v[156:159], v[66:69]
	v_mfma_f32_16x16x32_f16 v[6:9], v[176:179], v[156:159], v[6:9]
	v_mfma_f32_16x16x32_f16 v[10:13], v[184:187], v[138:141], v[10:13]
	v_mfma_f32_16x16x32_f16 v[18:21], v[184:187], v[156:159], v[18:21]
	v_mfma_f32_16x16x32_f16 v[30:33], v[196:199], v[138:141], v[30:33]
	s_barrier
	ds_read_b128 v[130:133], v161
	ds_read_b128 v[212:215], v162
	ds_read_b128 v[160:163], v163
	ds_read_b128 v[216:219], v164
	s_barrier
	s_waitcnt lgkmcnt(0)
	v_mfma_f32_16x16x32_f16 v[14:17], v[166:169], v[130:133], v[14:17]
	v_mfma_f32_16x16x32_f16 v[78:81], v[200:203], v[130:133], v[78:81]
	v_mfma_f32_16x16x32_f16 v[14:17], v[176:179], v[212:215], v[14:17]
	v_mfma_f32_16x16x32_f16 v[22:25], v[166:169], v[160:163], v[22:25]
	v_mfma_f32_16x16x32_f16 v[34:37], v[180:183], v[130:133], v[34:37]
	v_mfma_f32_16x16x32_f16 v[46:49], v[180:183], v[160:163], v[46:49]
	v_mfma_f32_16x16x32_f16 v[58:61], v[188:191], v[130:133], v[58:61]
	v_mfma_f32_16x16x32_f16 v[70:73], v[188:191], v[160:163], v[70:73]
	v_mfma_f32_16x16x32_f16 v[164:167], v[204:207], v[212:215], v[78:81]
	v_mfma_f32_16x16x32_f16 v[78:81], v[200:203], v[160:163], v[86:89]
	v_mfma_f32_16x16x32_f16 v[22:25], v[176:179], v[216:219], v[22:25]
	v_mfma_f32_16x16x32_f16 v[34:37], v[184:187], v[212:215], v[34:37]
	v_mfma_f32_16x16x32_f16 v[46:49], v[184:187], v[216:219], v[46:49]
	v_mfma_f32_16x16x32_f16 v[58:61], v[196:199], v[212:215], v[58:61]
	v_mfma_f32_16x16x32_f16 v[70:73], v[196:199], v[216:219], v[70:73]
	v_mfma_f32_16x16x32_f16 v[86:89], v[204:207], v[216:219], v[78:81]
	s_barrier
	s_nop 0
	ds_read_b128 v[78:81], v173 offset:16384
	ds_read_b128 v[168:171], v173 offset:17408
	ds_read_b128 v[174:177], v173 offset:18432
	ds_read_b128 v[178:181], v173 offset:19456
	ds_read_b128 v[182:185], v173 offset:20480
	ds_read_b128 v[186:189], v173 offset:21504
	ds_read_b128 v[190:193], v173 offset:22528
	ds_read_b128 v[196:199], v173 offset:23552
	s_waitcnt vmcnt(4)
	s_barrier
	s_waitcnt lgkmcnt(0)
	v_mfma_f32_16x16x32_f16 v[26:29], v[78:81], v[134:137], v[26:29]
	v_mfma_f32_16x16x32_f16 v[38:41], v[78:81], v[152:155], v[38:41]
	v_mfma_f32_16x16x32_f16 v[26:29], v[168:171], v[138:141], v[26:29]
	v_mfma_f32_16x16x32_f16 v[38:41], v[168:171], v[156:159], v[38:41]
	v_mfma_f32_16x16x32_f16 v[50:53], v[174:177], v[134:137], v[50:53]
	v_mfma_f32_16x16x32_f16 v[62:65], v[174:177], v[152:155], v[62:65]
	v_mfma_f32_16x16x32_f16 v[74:77], v[182:185], v[134:137], v[74:77]
	v_mfma_f32_16x16x32_f16 v[82:85], v[182:185], v[152:155], v[82:85]
	v_mfma_f32_16x16x32_f16 v[90:93], v[190:193], v[134:137], v[90:93]
	v_mfma_f32_16x16x32_f16 v[94:97], v[190:193], v[152:155], v[94:97]
	v_mfma_f32_16x16x32_f16 v[50:53], v[178:181], v[138:141], v[50:53]
	v_mfma_f32_16x16x32_f16 v[62:65], v[178:181], v[156:159], v[62:65]
	v_mfma_f32_16x16x32_f16 v[74:77], v[186:189], v[138:141], v[74:77]
	v_mfma_f32_16x16x32_f16 v[82:85], v[186:189], v[156:159], v[82:85]
	v_mfma_f32_16x16x32_f16 v[90:93], v[196:199], v[138:141], v[90:93]
	v_mfma_f32_16x16x32_f16 v[94:97], v[196:199], v[156:159], v[94:97]
	v_mfma_f32_16x16x32_f16 v[98:101], v[78:81], v[130:133], v[98:101]
	v_mfma_f32_16x16x32_f16 v[78:81], v[78:81], v[160:163], v[102:105]
	v_mfma_f32_16x16x32_f16 v[102:105], v[168:171], v[216:219], v[78:81]
	v_mfma_f32_16x16x32_f16 v[78:81], v[174:177], v[130:133], v[106:109]
	v_mfma_f32_16x16x32_f16 v[106:109], v[178:181], v[212:215], v[78:81]
	v_mfma_f32_16x16x32_f16 v[78:81], v[174:177], v[160:163], v[110:113]
	v_mfma_f32_16x16x32_f16 v[200:203], v[178:181], v[216:219], v[78:81]
	v_mfma_f32_16x16x32_f16 v[78:81], v[182:185], v[130:133], v[114:117]
	v_mfma_f32_16x16x32_f16 v[204:207], v[186:189], v[212:215], v[78:81]
	v_mfma_f32_16x16x32_f16 v[78:81], v[182:185], v[160:163], v[118:121]
	v_mfma_f32_16x16x32_f16 v[220:223], v[186:189], v[216:219], v[78:81]
	v_mfma_f32_16x16x32_f16 v[78:81], v[190:193], v[130:133], v[122:125]
	v_mfma_f32_16x16x32_f16 v[98:101], v[168:171], v[212:215], v[98:101]
	v_mfma_f32_16x16x32_f16 v[212:215], v[196:199], v[212:215], v[78:81]
	v_mfma_f32_16x16x32_f16 v[78:81], v[190:193], v[160:163], v[126:129]
	v_mfma_f32_16x16x32_f16 v[196:199], v[196:199], v[216:219], v[78:81]
	s_barrier
	ds_read_b128 v[110:113], v148
	ds_read_b128 v[130:133], v149
	ds_read_b128 v[216:219], v150
	ds_read_b128 v[224:227], v151
	s_nop 0
	ds_read_b128 v[78:81], v173 offset:32768
	ds_read_b128 v[114:117], v173 offset:33792
	ds_read_b128 v[118:121], v173 offset:34816
	ds_read_b128 v[134:137], v173 offset:35840
	ds_read_b128 v[138:141], v173 offset:36864
	ds_read_b128 v[168:171], v173 offset:37888
	ds_read_b128 v[174:177], v173 offset:38912
	ds_read_b128 v[228:231], v173 offset:39936
	s_waitcnt vmcnt(2)
	s_barrier
	s_waitcnt lgkmcnt(0)
	v_mfma_f32_16x16x32_f16 v[2:5], v[78:81], v[110:113], v[2:5]
	v_mfma_f32_16x16x32_f16 v[190:193], v[114:117], v[130:133], v[2:5]
	v_mfma_f32_16x16x32_f16 v[2:5], v[78:81], v[216:219], v[6:9]
	v_mfma_f32_16x16x32_f16 v[158:161], v[114:117], v[224:227], v[2:5]
	v_mfma_f32_16x16x32_f16 v[2:5], v[118:121], v[110:113], v[10:13]
	v_mfma_f32_16x16x32_f16 v[186:189], v[134:137], v[130:133], v[2:5]
	v_mfma_f32_16x16x32_f16 v[2:5], v[118:121], v[216:219], v[18:21]
	v_mfma_f32_16x16x32_f16 v[154:157], v[134:137], v[224:227], v[2:5]
	v_mfma_f32_16x16x32_f16 v[2:5], v[138:141], v[110:113], v[30:33]
	v_mfma_f32_16x16x32_f16 v[182:185], v[168:171], v[130:133], v[2:5]
	v_mfma_f32_16x16x32_f16 v[2:5], v[138:141], v[216:219], v[42:45]
	v_mfma_f32_16x16x32_f16 v[150:153], v[168:171], v[224:227], v[2:5]
	v_mfma_f32_16x16x32_f16 v[2:5], v[174:177], v[110:113], v[54:57]
	v_mfma_f32_16x16x32_f16 v[178:181], v[228:231], v[130:133], v[2:5]
	v_mfma_f32_16x16x32_f16 v[2:5], v[174:177], v[216:219], v[66:69]
	v_mfma_f32_16x16x32_f16 v[146:149], v[228:231], v[224:227], v[2:5]
	s_barrier
	s_nop 4
	ds_read_b128 v[2:5], v142
	ds_read_b128 v[6:9], v143
	ds_read_b128 v[10:13], v144
	ds_read_b128 v[18:21], v145
	s_waitcnt vmcnt(0)
	s_barrier
	s_waitcnt lgkmcnt(0)
	v_mfma_f32_16x16x32_f16 v[14:17], v[78:81], v[2:5], v[14:17]
	v_mfma_f32_16x16x32_f16 v[126:129], v[114:117], v[6:9], v[14:17]
	v_mfma_f32_16x16x32_f16 v[14:17], v[78:81], v[10:13], v[22:25]
	v_mfma_f32_16x16x32_f16 v[78:81], v[114:117], v[18:21], v[14:17]
	v_mfma_f32_16x16x32_f16 v[14:17], v[118:121], v[2:5], v[34:37]
	v_mfma_f32_16x16x32_f16 v[122:125], v[134:137], v[6:9], v[14:17]
	v_mfma_f32_16x16x32_f16 v[14:17], v[118:121], v[10:13], v[46:49]
	v_mfma_f32_16x16x32_f16 v[66:69], v[134:137], v[18:21], v[14:17]
	v_mfma_f32_16x16x32_f16 v[14:17], v[138:141], v[2:5], v[58:61]
	v_mfma_f32_16x16x32_f16 v[118:121], v[168:171], v[6:9], v[14:17]
	v_mfma_f32_16x16x32_f16 v[14:17], v[138:141], v[10:13], v[70:73]
	v_mfma_f32_16x16x32_f16 v[54:57], v[168:171], v[18:21], v[14:17]
	v_mfma_f32_16x16x32_f16 v[14:17], v[174:177], v[2:5], v[164:167]
	v_mfma_f32_16x16x32_f16 v[114:117], v[228:231], v[6:9], v[14:17]
	v_mfma_f32_16x16x32_f16 v[14:17], v[174:177], v[10:13], v[86:89]
	v_mfma_f32_16x16x32_f16 v[42:45], v[228:231], v[18:21], v[14:17]
	s_barrier
	s_nop 4
	ds_read_b128 v[14:17], v173 offset:49152
	ds_read_b128 v[22:25], v173 offset:50176
	ds_read_b128 v[30:33], v173 offset:51200
	ds_read_b128 v[34:37], v173 offset:52224
	ds_read_b128 v[46:49], v173 offset:53248
	ds_read_b128 v[58:61], v173 offset:54272
	ds_read_b128 v[70:73], v173 offset:55296
	ds_read_b128 v[86:89], v173 offset:56320
	s_barrier
	s_waitcnt lgkmcnt(0)
	v_mfma_f32_16x16x32_f16 v[26:29], v[14:17], v[110:113], v[26:29]
	v_mfma_f32_16x16x32_f16 v[174:177], v[22:25], v[130:133], v[26:29]
	v_mfma_f32_16x16x32_f16 v[26:29], v[14:17], v[216:219], v[38:41]
	v_mfma_f32_16x16x32_f16 v[142:145], v[22:25], v[224:227], v[26:29]
	v_mfma_f32_16x16x32_f16 v[26:29], v[30:33], v[110:113], v[50:53]
	v_mfma_f32_16x16x32_f16 v[170:173], v[34:37], v[130:133], v[26:29]
	v_mfma_f32_16x16x32_f16 v[26:29], v[30:33], v[216:219], v[62:65]
	v_mfma_f32_16x16x32_f16 v[138:141], v[34:37], v[224:227], v[26:29]
	v_mfma_f32_16x16x32_f16 v[26:29], v[46:49], v[110:113], v[74:77]
	v_mfma_f32_16x16x32_f16 v[166:169], v[58:61], v[130:133], v[26:29]
	v_mfma_f32_16x16x32_f16 v[26:29], v[46:49], v[216:219], v[82:85]
	v_mfma_f32_16x16x32_f16 v[134:137], v[58:61], v[224:227], v[26:29]
	v_mfma_f32_16x16x32_f16 v[26:29], v[70:73], v[110:113], v[90:93]
	v_mfma_f32_16x16x32_f16 v[162:165], v[86:89], v[130:133], v[26:29]
	v_mfma_f32_16x16x32_f16 v[26:29], v[70:73], v[216:219], v[94:97]
	v_mfma_f32_16x16x32_f16 v[130:133], v[86:89], v[224:227], v[26:29]
	v_mfma_f32_16x16x32_f16 v[26:29], v[14:17], v[2:5], v[98:101]
	v_mfma_f32_16x16x32_f16 v[14:17], v[14:17], v[10:13], v[102:105]
	v_mfma_f32_16x16x32_f16 v[38:41], v[22:25], v[18:21], v[14:17]
	v_mfma_f32_16x16x32_f16 v[14:17], v[30:33], v[2:5], v[106:109]
	v_mfma_f32_16x16x32_f16 v[106:109], v[34:37], v[6:9], v[14:17]
	v_mfma_f32_16x16x32_f16 v[14:17], v[30:33], v[10:13], v[200:203]
	v_mfma_f32_16x16x32_f16 v[110:113], v[22:25], v[6:9], v[26:29]
	v_mfma_f32_16x16x32_f16 v[26:29], v[34:37], v[18:21], v[14:17]
	v_mfma_f32_16x16x32_f16 v[14:17], v[46:49], v[2:5], v[204:207]
	v_mfma_f32_16x16x32_f16 v[2:5], v[70:73], v[2:5], v[212:215]
	v_mfma_f32_16x16x32_f16 v[102:105], v[58:61], v[6:9], v[14:17]
	v_mfma_f32_16x16x32_f16 v[14:17], v[46:49], v[10:13], v[220:223]
	v_mfma_f32_16x16x32_f16 v[98:101], v[86:89], v[6:9], v[2:5]
	v_mfma_f32_16x16x32_f16 v[2:5], v[70:73], v[10:13], v[196:199]
	v_mfma_f32_16x16x32_f16 v[14:17], v[58:61], v[18:21], v[14:17]
	v_mfma_f32_16x16x32_f16 v[2:5], v[86:89], v[18:21], v[2:5]
	s_cmpk_gt_u32 s65, 0xff
	s_barrier
	s_cbranch_scc1 .LBB6_15
	s_barrier

.LBB7_239:
	ds_read_b128 v[176:179], v169
	ds_read_b128 v[180:183], v170
	ds_read_b128 v[184:187], v171
	ds_read_b128 v[188:191], v172
	v_add_u32_e32 v174, 0xc000, v152
	v_lshl_add_u64 v[192:193], v[136:137], 0, s[46:47]
	v_add_u32_e32 v175, 0xe000, v152
	v_add_u32_e32 v173, s5, v168
	v_lshl_add_u64 v[232:233], v[192:193], 0, s[34:35]
	s_mov_b32 m0, s72
	v_lshl_add_u64 v[248:249], v[134:135], 0, s[46:47]
	ds_read_b128 v[196:199], v173
	ds_read_b128 v[200:203], v173 offset:1024
	ds_read_b128 v[204:207], v173 offset:2048
	ds_read_b128 v[212:215], v173 offset:3072
	ds_read_b128 v[216:219], v173 offset:4096
	ds_read_b128 v[220:223], v173 offset:5120
	ds_read_b128 v[224:227], v173 offset:6144
	ds_read_b128 v[228:231], v173 offset:7168
	global_load_lds_dwordx4 v[232:233], off
	s_mov_b32 m0, s73
	v_lshl_add_u64 v[232:233], v[248:249], 0, s[34:35]
	global_load_lds_dwordx4 v[232:233], off
	s_waitcnt lgkmcnt(8)
	s_barrier
	s_waitcnt lgkmcnt(0)
	v_mfma_f32_16x16x32_f16 v[2:5], v[196:199], v[176:179], v[2:5]
	v_mfma_f32_16x16x32_f16 v[6:9], v[196:199], v[184:187], v[6:9]
	v_mfma_f32_16x16x32_f16 v[10:13], v[204:207], v[176:179], v[10:13]
	v_mfma_f32_16x16x32_f16 v[18:21], v[204:207], v[184:187], v[18:21]
	v_mfma_f32_16x16x32_f16 v[30:33], v[216:219], v[176:179], v[30:33]
	v_mfma_f32_16x16x32_f16 v[42:45], v[216:219], v[184:187], v[42:45]
	v_mfma_f32_16x16x32_f16 v[54:57], v[224:227], v[176:179], v[54:57]
	v_mfma_f32_16x16x32_f16 v[66:69], v[224:227], v[184:187], v[66:69]
	v_mfma_f32_16x16x32_f16 v[2:5], v[200:203], v[180:183], v[2:5]
	v_mfma_f32_16x16x32_f16 v[6:9], v[200:203], v[188:191], v[6:9]
	v_mfma_f32_16x16x32_f16 v[10:13], v[212:215], v[180:183], v[10:13]
	v_mfma_f32_16x16x32_f16 v[18:21], v[212:215], v[188:191], v[18:21]
	v_mfma_f32_16x16x32_f16 v[30:33], v[220:223], v[180:183], v[30:33]
	v_mfma_f32_16x16x32_f16 v[42:45], v[220:223], v[188:191], v[42:45]
	v_mfma_f32_16x16x32_f16 v[54:57], v[228:231], v[180:183], v[54:57]
	v_mfma_f32_16x16x32_f16 v[66:69], v[228:231], v[188:191], v[66:69]
	s_barrier
	v_lshl_add_u64 v[250:251], v[140:141], 0, s[46:47]
	v_lshl_add_u64 v[252:253], v[250:251], 0, s[36:37]
	s_mov_b32 m0, s74
	ds_read_b128 v[232:235], v161
	ds_read_b128 v[236:239], v162
	ds_read_b128 v[240:243], v163
	ds_read_b128 v[244:247], v164
	global_load_lds_dwordx4 v[252:253], off
	v_lshl_add_u64 v[252:253], v[138:139], 0, s[46:47]
	s_mov_b32 m0, s75
	v_lshl_add_u64 v[254:255], v[252:253], 0, s[36:37]
	global_load_lds_dwordx4 v[254:255], off
	s_barrier
	s_waitcnt lgkmcnt(0)
	v_mfma_f32_16x16x32_f16 v[14:17], v[196:199], v[232:235], v[14:17]
	v_mfma_f32_16x16x32_f16 v[22:25], v[196:199], v[240:243], v[22:25]
	v_mfma_f32_16x16x32_f16 v[34:37], v[204:207], v[232:235], v[34:37]
	v_mfma_f32_16x16x32_f16 v[46:49], v[204:207], v[240:243], v[46:49]
	v_mfma_f32_16x16x32_f16 v[58:61], v[216:219], v[232:235], v[58:61]
	v_mfma_f32_16x16x32_f16 v[70:73], v[216:219], v[240:243], v[70:73]
	v_mfma_f32_16x16x32_f16 v[78:81], v[224:227], v[232:235], v[78:81]
	v_mfma_f32_16x16x32_f16 v[86:89], v[224:227], v[240:243], v[86:89]
	v_mfma_f32_16x16x32_f16 v[14:17], v[200:203], v[236:239], v[14:17]
	v_mfma_f32_16x16x32_f16 v[22:25], v[200:203], v[244:247], v[22:25]
	v_mfma_f32_16x16x32_f16 v[34:37], v[212:215], v[236:239], v[34:37]
	v_mfma_f32_16x16x32_f16 v[46:49], v[212:215], v[244:247], v[46:49]
	v_mfma_f32_16x16x32_f16 v[58:61], v[220:223], v[236:239], v[58:61]
	v_mfma_f32_16x16x32_f16 v[70:73], v[220:223], v[244:247], v[70:73]
	v_mfma_f32_16x16x32_f16 v[78:81], v[228:231], v[236:239], v[78:81]
	v_mfma_f32_16x16x32_f16 v[86:89], v[228:231], v[244:247], v[86:89]
	v_lshl_add_u64 v[254:255], v[192:193], 0, s[36:37]
	s_mov_b32 m0, s76
	s_barrier
	ds_read_b128 v[196:199], v173 offset:16384
	ds_read_b128 v[200:203], v173 offset:17408
	ds_read_b128 v[204:207], v173 offset:18432
	ds_read_b128 v[212:215], v173 offset:19456
	ds_read_b128 v[216:219], v173 offset:20480
	ds_read_b128 v[220:223], v173 offset:21504
	ds_read_b128 v[224:227], v173 offset:22528
	ds_read_b128 v[228:231], v173 offset:23552
	global_load_lds_dwordx4 v[254:255], off
	s_mov_b32 m0, s77
	v_lshl_add_u64 v[254:255], v[248:249], 0, s[36:37]
	global_load_lds_dwordx4 v[254:255], off
	s_barrier
	s_waitcnt lgkmcnt(0)
	v_mfma_f32_16x16x32_f16 v[26:29], v[196:199], v[176:179], v[26:29]
	v_mfma_f32_16x16x32_f16 v[38:41], v[196:199], v[184:187], v[38:41]
	v_mfma_f32_16x16x32_f16 v[50:53], v[204:207], v[176:179], v[50:53]
	v_mfma_f32_16x16x32_f16 v[62:65], v[204:207], v[184:187], v[62:65]
	v_mfma_f32_16x16x32_f16 v[74:77], v[216:219], v[176:179], v[74:77]
	v_mfma_f32_16x16x32_f16 v[82:85], v[216:219], v[184:187], v[82:85]
	v_mfma_f32_16x16x32_f16 v[90:93], v[224:227], v[176:179], v[90:93]
	v_mfma_f32_16x16x32_f16 v[94:97], v[224:227], v[184:187], v[94:97]
	v_mfma_f32_16x16x32_f16 v[26:29], v[200:203], v[180:183], v[26:29]
	v_mfma_f32_16x16x32_f16 v[38:41], v[200:203], v[188:191], v[38:41]
	v_mfma_f32_16x16x32_f16 v[50:53], v[212:215], v[180:183], v[50:53]
	v_mfma_f32_16x16x32_f16 v[62:65], v[212:215], v[188:191], v[62:65]
	v_mfma_f32_16x16x32_f16 v[74:77], v[220:223], v[180:183], v[74:77]
	v_mfma_f32_16x16x32_f16 v[82:85], v[220:223], v[188:191], v[82:85]
	v_mfma_f32_16x16x32_f16 v[90:93], v[228:231], v[180:183], v[90:93]
	v_mfma_f32_16x16x32_f16 v[94:97], v[228:231], v[188:191], v[94:97]
	s_barrier
	s_mov_b32 m0, s78
	v_lshl_add_u64 v[176:177], v[250:251], 0, s[38:39]
	global_load_lds_dwordx4 v[176:177], off
	s_mov_b32 m0, s79
	v_lshl_add_u64 v[176:177], v[252:253], 0, s[38:39]
	global_load_lds_dwordx4 v[176:177], off
	s_waitcnt vmcnt(6)
	s_barrier
	v_mfma_f32_16x16x32_f16 v[98:101], v[196:199], v[232:235], v[98:101]
	v_mfma_f32_16x16x32_f16 v[102:105], v[196:199], v[240:243], v[102:105]
	v_mfma_f32_16x16x32_f16 v[106:109], v[204:207], v[232:235], v[106:109]
	v_mfma_f32_16x16x32_f16 v[110:113], v[204:207], v[240:243], v[110:113]
	v_mfma_f32_16x16x32_f16 v[114:117], v[216:219], v[232:235], v[114:117]
	v_mfma_f32_16x16x32_f16 v[118:121], v[216:219], v[240:243], v[118:121]
	v_mfma_f32_16x16x32_f16 v[122:125], v[224:227], v[232:235], v[122:125]
	v_mfma_f32_16x16x32_f16 v[126:129], v[224:227], v[240:243], v[126:129]
	v_mfma_f32_16x16x32_f16 v[98:101], v[200:203], v[236:239], v[98:101]
	v_mfma_f32_16x16x32_f16 v[102:105], v[200:203], v[244:247], v[102:105]
	v_mfma_f32_16x16x32_f16 v[106:109], v[212:215], v[236:239], v[106:109]
	v_mfma_f32_16x16x32_f16 v[110:113], v[212:215], v[244:247], v[110:113]
	v_mfma_f32_16x16x32_f16 v[114:117], v[220:223], v[236:239], v[114:117]
	v_mfma_f32_16x16x32_f16 v[118:121], v[220:223], v[244:247], v[118:121]
	v_mfma_f32_16x16x32_f16 v[122:125], v[228:231], v[236:239], v[122:125]
	v_mfma_f32_16x16x32_f16 v[126:129], v[228:231], v[244:247], v[126:129]
	s_barrier
	ds_read_b128 v[176:179], v148
	ds_read_b128 v[180:183], v149
	ds_read_b128 v[184:187], v150
	ds_read_b128 v[188:191], v151
	v_lshl_add_u64 v[232:233], v[192:193], 0, s[38:39]
	s_mov_b32 m0, s80
	ds_read_b128 v[196:199], v173 offset:32768
	ds_read_b128 v[200:203], v173 offset:33792
	ds_read_b128 v[204:207], v173 offset:34816
	ds_read_b128 v[212:215], v173 offset:35840
	ds_read_b128 v[216:219], v173 offset:36864
	ds_read_b128 v[220:223], v173 offset:37888
	ds_read_b128 v[224:227], v173 offset:38912
	ds_read_b128 v[228:231], v173 offset:39936
	global_load_lds_dwordx4 v[232:233], off
	s_mov_b32 m0, s81
	v_lshl_add_u64 v[232:233], v[248:249], 0, s[38:39]
	global_load_lds_dwordx4 v[232:233], off
	s_waitcnt lgkmcnt(8)
	s_barrier
	s_waitcnt lgkmcnt(0)
	v_mfma_f32_16x16x32_f16 v[2:5], v[196:199], v[176:179], v[2:5]
	v_mfma_f32_16x16x32_f16 v[6:9], v[196:199], v[184:187], v[6:9]
	v_mfma_f32_16x16x32_f16 v[10:13], v[204:207], v[176:179], v[10:13]
	v_mfma_f32_16x16x32_f16 v[18:21], v[204:207], v[184:187], v[18:21]
	v_mfma_f32_16x16x32_f16 v[30:33], v[216:219], v[176:179], v[30:33]
	v_mfma_f32_16x16x32_f16 v[42:45], v[216:219], v[184:187], v[42:45]
	v_mfma_f32_16x16x32_f16 v[54:57], v[224:227], v[176:179], v[54:57]
	v_mfma_f32_16x16x32_f16 v[66:69], v[224:227], v[184:187], v[66:69]
	v_mfma_f32_16x16x32_f16 v[2:5], v[200:203], v[180:183], v[2:5]
	v_mfma_f32_16x16x32_f16 v[6:9], v[200:203], v[188:191], v[6:9]
	v_mfma_f32_16x16x32_f16 v[10:13], v[212:215], v[180:183], v[10:13]
	v_mfma_f32_16x16x32_f16 v[18:21], v[212:215], v[188:191], v[18:21]
	v_mfma_f32_16x16x32_f16 v[30:33], v[220:223], v[180:183], v[30:33]
	v_mfma_f32_16x16x32_f16 v[42:45], v[220:223], v[188:191], v[42:45]
	v_mfma_f32_16x16x32_f16 v[54:57], v[228:231], v[180:183], v[54:57]
	v_mfma_f32_16x16x32_f16 v[66:69], v[228:231], v[188:191], v[66:69]
	s_barrier
	v_lshl_add_u64 v[254:255], v[250:251], 0, s[40:41]
	s_mov_b32 m0, s82
	ds_read_b128 v[232:235], v142
	ds_read_b128 v[236:239], v143
	ds_read_b128 v[240:243], v144
	ds_read_b128 v[244:247], v145
	global_load_lds_dwordx4 v[254:255], off
	s_mov_b32 m0, s83
	v_lshl_add_u64 v[254:255], v[252:253], 0, s[40:41]
	global_load_lds_dwordx4 v[254:255], off
	s_barrier
	s_waitcnt lgkmcnt(0)
	v_mfma_f32_16x16x32_f16 v[14:17], v[196:199], v[232:235], v[14:17]
	v_mfma_f32_16x16x32_f16 v[22:25], v[196:199], v[240:243], v[22:25]
	v_mfma_f32_16x16x32_f16 v[34:37], v[204:207], v[232:235], v[34:37]
	v_mfma_f32_16x16x32_f16 v[46:49], v[204:207], v[240:243], v[46:49]
	v_mfma_f32_16x16x32_f16 v[58:61], v[216:219], v[232:235], v[58:61]
	v_mfma_f32_16x16x32_f16 v[70:73], v[216:219], v[240:243], v[70:73]
	v_mfma_f32_16x16x32_f16 v[78:81], v[224:227], v[232:235], v[78:81]
	v_mfma_f32_16x16x32_f16 v[86:89], v[224:227], v[240:243], v[86:89]
	v_mfma_f32_16x16x32_f16 v[14:17], v[200:203], v[236:239], v[14:17]
	v_mfma_f32_16x16x32_f16 v[22:25], v[200:203], v[244:247], v[22:25]
	v_mfma_f32_16x16x32_f16 v[34:37], v[212:215], v[236:239], v[34:37]
	v_mfma_f32_16x16x32_f16 v[46:49], v[212:215], v[244:247], v[46:49]
	v_mfma_f32_16x16x32_f16 v[58:61], v[220:223], v[236:239], v[58:61]
	v_mfma_f32_16x16x32_f16 v[70:73], v[220:223], v[244:247], v[70:73]
	v_mfma_f32_16x16x32_f16 v[78:81], v[228:231], v[236:239], v[78:81]
	v_mfma_f32_16x16x32_f16 v[86:89], v[228:231], v[244:247], v[86:89]
	v_lshl_add_u64 v[192:193], v[192:193], 0, s[40:41]
	s_mov_b32 m0, s84
	s_barrier
	ds_read_b128 v[196:199], v173 offset:49152
	ds_read_b128 v[200:203], v173 offset:50176
	ds_read_b128 v[204:207], v173 offset:51200
	ds_read_b128 v[212:215], v173 offset:52224
	ds_read_b128 v[216:219], v173 offset:53248
	ds_read_b128 v[220:223], v173 offset:54272
	ds_read_b128 v[224:227], v173 offset:55296
	ds_read_b128 v[228:231], v173 offset:56320
	global_load_lds_dwordx4 v[192:193], off
	s_mov_b32 m0, s85
	v_lshl_add_u64 v[192:193], v[248:249], 0, s[40:41]
	global_load_lds_dwordx4 v[192:193], off
	s_barrier
	s_waitcnt lgkmcnt(0)
	v_mfma_f32_16x16x32_f16 v[26:29], v[196:199], v[176:179], v[26:29]
	v_mfma_f32_16x16x32_f16 v[38:41], v[196:199], v[184:187], v[38:41]
	v_mfma_f32_16x16x32_f16 v[50:53], v[204:207], v[176:179], v[50:53]
	v_mfma_f32_16x16x32_f16 v[62:65], v[204:207], v[184:187], v[62:65]
	v_mfma_f32_16x16x32_f16 v[74:77], v[216:219], v[176:179], v[74:77]
	v_mfma_f32_16x16x32_f16 v[82:85], v[216:219], v[184:187], v[82:85]
	v_mfma_f32_16x16x32_f16 v[90:93], v[224:227], v[176:179], v[90:93]
	v_mfma_f32_16x16x32_f16 v[94:97], v[224:227], v[184:187], v[94:97]
	v_mfma_f32_16x16x32_f16 v[26:29], v[200:203], v[180:183], v[26:29]
	v_mfma_f32_16x16x32_f16 v[38:41], v[200:203], v[188:191], v[38:41]
	v_mfma_f32_16x16x32_f16 v[50:53], v[212:215], v[180:183], v[50:53]
	v_mfma_f32_16x16x32_f16 v[62:65], v[212:215], v[188:191], v[62:65]
	v_mfma_f32_16x16x32_f16 v[74:77], v[220:223], v[180:183], v[74:77]
	v_mfma_f32_16x16x32_f16 v[82:85], v[220:223], v[188:191], v[82:85]
	v_mfma_f32_16x16x32_f16 v[90:93], v[228:231], v[180:183], v[90:93]
	v_mfma_f32_16x16x32_f16 v[94:97], v[228:231], v[188:191], v[94:97]
	s_barrier
	s_mov_b32 m0, s86
	v_lshl_add_u64 v[176:177], v[250:251], 0, s[42:43]
	global_load_lds_dwordx4 v[176:177], off
	s_mov_b32 m0, s87
	v_lshl_add_u64 v[176:177], v[252:253], 0, s[42:43]
	global_load_lds_dwordx4 v[176:177], off
	s_waitcnt vmcnt(6)
	s_barrier
	v_mfma_f32_16x16x32_f16 v[98:101], v[196:199], v[232:235], v[98:101]
	v_mfma_f32_16x16x32_f16 v[102:105], v[196:199], v[240:243], v[102:105]
	v_mfma_f32_16x16x32_f16 v[106:109], v[204:207], v[232:235], v[106:109]
	v_mfma_f32_16x16x32_f16 v[110:113], v[204:207], v[240:243], v[110:113]
	v_mfma_f32_16x16x32_f16 v[114:117], v[216:219], v[232:235], v[114:117]
	v_mfma_f32_16x16x32_f16 v[118:121], v[216:219], v[240:243], v[118:121]
	v_mfma_f32_16x16x32_f16 v[122:125], v[224:227], v[232:235], v[122:125]
	v_mfma_f32_16x16x32_f16 v[126:129], v[224:227], v[240:243], v[126:129]
	v_mfma_f32_16x16x32_f16 v[98:101], v[200:203], v[236:239], v[98:101]
	v_mfma_f32_16x16x32_f16 v[102:105], v[200:203], v[244:247], v[102:105]
	v_mfma_f32_16x16x32_f16 v[106:109], v[212:215], v[236:239], v[106:109]
	v_mfma_f32_16x16x32_f16 v[110:113], v[212:215], v[244:247], v[110:113]
	v_mfma_f32_16x16x32_f16 v[114:117], v[220:223], v[236:239], v[114:117]
	v_mfma_f32_16x16x32_f16 v[118:121], v[220:223], v[244:247], v[118:121]
	v_mfma_f32_16x16x32_f16 v[122:125], v[228:231], v[236:239], v[122:125]
	v_mfma_f32_16x16x32_f16 v[126:129], v[228:231], v[244:247], v[126:129]
	s_add_i32 s48, s48, 2
	s_add_u32 s46, s46, 0x100
	s_addc_u32 s47, s47, 0
	s_cmp_lt_u32 s48, 4
	s_barrier
	s_cbranch_scc1 .LBB7_239
	s_add_u32 s0, s0, 0x20380
	s_addc_u32 s1, s1, 0
	v_readfirstlane_b32 s5, v174
	v_lshl_add_u64 v[130:131], v[130:131], 1, s[0:1]
	s_mov_b32 m0, s5
	ds_read_b128 v[134:137], v169
	ds_read_b128 v[138:141], v170
	ds_read_b128 v[152:155], v171
	ds_read_b128 v[156:159], v172
	ds_read_b128 v[166:169], v173
	ds_read_b128 v[176:179], v173 offset:1024
	ds_read_b128 v[180:183], v173 offset:2048
	ds_read_b128 v[184:187], v173 offset:3072
	ds_read_b128 v[188:191], v173 offset:4096
	ds_read_b128 v[196:199], v173 offset:5120
	ds_read_b128 v[200:203], v173 offset:6144
	ds_read_b128 v[204:207], v173 offset:7168
	global_load_lds_dwordx4 v[130:131], off
	v_lshl_add_u64 v[130:131], v[132:133], 1, s[0:1]
	v_readfirstlane_b32 s0, v175
	s_mov_b32 m0, s0
	s_nop 0
	global_load_lds_dwordx4 v[130:131], off
	s_barrier
	s_waitcnt lgkmcnt(0)
	v_mfma_f32_16x16x32_f16 v[2:5], v[166:169], v[134:137], v[2:5]
	v_mfma_f32_16x16x32_f16 v[42:45], v[188:191], v[152:155], v[42:45]
	v_mfma_f32_16x16x32_f16 v[54:57], v[200:203], v[134:137], v[54:57]
	v_mfma_f32_16x16x32_f16 v[66:69], v[200:203], v[152:155], v[66:69]
	v_mfma_f32_16x16x32_f16 v[2:5], v[176:179], v[138:141], v[2:5]
	v_mfma_f32_16x16x32_f16 v[6:9], v[166:169], v[152:155], v[6:9]
	v_mfma_f32_16x16x32_f16 v[10:13], v[180:183], v[134:137], v[10:13]
	v_mfma_f32_16x16x32_f16 v[18:21], v[180:183], v[152:155], v[18:21]
	v_mfma_f32_16x16x32_f16 v[30:33], v[188:191], v[134:137], v[30:33]
	v_mfma_f32_16x16x32_f16 v[42:45], v[196:199], v[156:159], v[42:45]
	v_mfma_f32_16x16x32_f16 v[54:57], v[204:207], v[138:141], v[54:57]
	v_mfma_f32_16x16x32_f16 v[66:69], v[204:207], v[156:159], v[66:69]
	v_mfma_f32_16x16x32_f16 v[6:9], v[176:179], v[156:159], v[6:9]
	v_mfma_f32_16x16x32_f16 v[10:13], v[184:187], v[138:141], v[10:13]
	v_mfma_f32_16x16x32_f16 v[18:21], v[184:187], v[156:159], v[18:21]
	v_mfma_f32_16x16x32_f16 v[30:33], v[196:199], v[138:141], v[30:33]
	s_barrier
	ds_read_b128 v[130:133], v161
	ds_read_b128 v[212:215], v162
	ds_read_b128 v[160:163], v163
	ds_read_b128 v[216:219], v164
	s_barrier
	s_waitcnt lgkmcnt(0)
	v_mfma_f32_16x16x32_f16 v[14:17], v[166:169], v[130:133], v[14:17]
	v_mfma_f32_16x16x32_f16 v[78:81], v[200:203], v[130:133], v[78:81]
	v_mfma_f32_16x16x32_f16 v[14:17], v[176:179], v[212:215], v[14:17]
	v_mfma_f32_16x16x32_f16 v[22:25], v[166:169], v[160:163], v[22:25]
	v_mfma_f32_16x16x32_f16 v[34:37], v[180:183], v[130:133], v[34:37]
	v_mfma_f32_16x16x32_f16 v[46:49], v[180:183], v[160:163], v[46:49]
	v_mfma_f32_16x16x32_f16 v[58:61], v[188:191], v[130:133], v[58:61]
	v_mfma_f32_16x16x32_f16 v[70:73], v[188:191], v[160:163], v[70:73]
	v_mfma_f32_16x16x32_f16 v[164:167], v[204:207], v[212:215], v[78:81]
	v_mfma_f32_16x16x32_f16 v[78:81], v[200:203], v[160:163], v[86:89]
	v_mfma_f32_16x16x32_f16 v[22:25], v[176:179], v[216:219], v[22:25]
	v_mfma_f32_16x16x32_f16 v[34:37], v[184:187], v[212:215], v[34:37]
	v_mfma_f32_16x16x32_f16 v[46:49], v[184:187], v[216:219], v[46:49]
	v_mfma_f32_16x16x32_f16 v[58:61], v[196:199], v[212:215], v[58:61]
	v_mfma_f32_16x16x32_f16 v[70:73], v[196:199], v[216:219], v[70:73]
	v_mfma_f32_16x16x32_f16 v[86:89], v[204:207], v[216:219], v[78:81]
	s_barrier
	s_nop 0
	ds_read_b128 v[78:81], v173 offset:16384
	ds_read_b128 v[168:171], v173 offset:17408
	ds_read_b128 v[174:177], v173 offset:18432
	ds_read_b128 v[178:181], v173 offset:19456
	ds_read_b128 v[182:185], v173 offset:20480
	ds_read_b128 v[186:189], v173 offset:21504
	ds_read_b128 v[190:193], v173 offset:22528
	ds_read_b128 v[196:199], v173 offset:23552
	s_waitcnt vmcnt(4)
	s_barrier
	s_waitcnt lgkmcnt(0)
	v_mfma_f32_16x16x32_f16 v[26:29], v[78:81], v[134:137], v[26:29]
	v_mfma_f32_16x16x32_f16 v[38:41], v[78:81], v[152:155], v[38:41]
	v_mfma_f32_16x16x32_f16 v[26:29], v[168:171], v[138:141], v[26:29]
	v_mfma_f32_16x16x32_f16 v[38:41], v[168:171], v[156:159], v[38:41]
	v_mfma_f32_16x16x32_f16 v[50:53], v[174:177], v[134:137], v[50:53]
	v_mfma_f32_16x16x32_f16 v[62:65], v[174:177], v[152:155], v[62:65]
	v_mfma_f32_16x16x32_f16 v[74:77], v[182:185], v[134:137], v[74:77]
	v_mfma_f32_16x16x32_f16 v[82:85], v[182:185], v[152:155], v[82:85]
	v_mfma_f32_16x16x32_f16 v[90:93], v[190:193], v[134:137], v[90:93]
	v_mfma_f32_16x16x32_f16 v[94:97], v[190:193], v[152:155], v[94:97]
	v_mfma_f32_16x16x32_f16 v[50:53], v[178:181], v[138:141], v[50:53]
	v_mfma_f32_16x16x32_f16 v[62:65], v[178:181], v[156:159], v[62:65]
	v_mfma_f32_16x16x32_f16 v[74:77], v[186:189], v[138:141], v[74:77]
	v_mfma_f32_16x16x32_f16 v[82:85], v[186:189], v[156:159], v[82:85]
	v_mfma_f32_16x16x32_f16 v[90:93], v[196:199], v[138:141], v[90:93]
	v_mfma_f32_16x16x32_f16 v[94:97], v[196:199], v[156:159], v[94:97]
	v_mfma_f32_16x16x32_f16 v[98:101], v[78:81], v[130:133], v[98:101]
	v_mfma_f32_16x16x32_f16 v[78:81], v[78:81], v[160:163], v[102:105]
	v_mfma_f32_16x16x32_f16 v[102:105], v[168:171], v[216:219], v[78:81]
	v_mfma_f32_16x16x32_f16 v[78:81], v[174:177], v[130:133], v[106:109]
	v_mfma_f32_16x16x32_f16 v[106:109], v[178:181], v[212:215], v[78:81]
	v_mfma_f32_16x16x32_f16 v[78:81], v[174:177], v[160:163], v[110:113]
	v_mfma_f32_16x16x32_f16 v[200:203], v[178:181], v[216:219], v[78:81]
	v_mfma_f32_16x16x32_f16 v[78:81], v[182:185], v[130:133], v[114:117]
	v_mfma_f32_16x16x32_f16 v[204:207], v[186:189], v[212:215], v[78:81]
	v_mfma_f32_16x16x32_f16 v[78:81], v[182:185], v[160:163], v[118:121]
	v_mfma_f32_16x16x32_f16 v[220:223], v[186:189], v[216:219], v[78:81]
	v_mfma_f32_16x16x32_f16 v[78:81], v[190:193], v[130:133], v[122:125]
	v_mfma_f32_16x16x32_f16 v[98:101], v[168:171], v[212:215], v[98:101]
	v_mfma_f32_16x16x32_f16 v[212:215], v[196:199], v[212:215], v[78:81]
	v_mfma_f32_16x16x32_f16 v[78:81], v[190:193], v[160:163], v[126:129]
	v_mfma_f32_16x16x32_f16 v[196:199], v[196:199], v[216:219], v[78:81]
	s_barrier
	ds_read_b128 v[110:113], v148
	ds_read_b128 v[130:133], v149
	ds_read_b128 v[216:219], v150
	ds_read_b128 v[224:227], v151
	s_nop 0
	ds_read_b128 v[78:81], v173 offset:32768
	ds_read_b128 v[114:117], v173 offset:33792
	ds_read_b128 v[118:121], v173 offset:34816
	ds_read_b128 v[134:137], v173 offset:35840
	ds_read_b128 v[138:141], v173 offset:36864
	ds_read_b128 v[168:171], v173 offset:37888
	ds_read_b128 v[174:177], v173 offset:38912
	ds_read_b128 v[228:231], v173 offset:39936
	s_waitcnt vmcnt(2)
	s_barrier
	s_waitcnt lgkmcnt(0)
	v_mfma_f32_16x16x32_f16 v[2:5], v[78:81], v[110:113], v[2:5]
	v_mfma_f32_16x16x32_f16 v[190:193], v[114:117], v[130:133], v[2:5]
	v_mfma_f32_16x16x32_f16 v[2:5], v[78:81], v[216:219], v[6:9]
	v_mfma_f32_16x16x32_f16 v[158:161], v[114:117], v[224:227], v[2:5]
	v_mfma_f32_16x16x32_f16 v[2:5], v[118:121], v[110:113], v[10:13]
	v_mfma_f32_16x16x32_f16 v[186:189], v[134:137], v[130:133], v[2:5]
	v_mfma_f32_16x16x32_f16 v[2:5], v[118:121], v[216:219], v[18:21]
	v_mfma_f32_16x16x32_f16 v[154:157], v[134:137], v[224:227], v[2:5]
	v_mfma_f32_16x16x32_f16 v[2:5], v[138:141], v[110:113], v[30:33]
	v_mfma_f32_16x16x32_f16 v[182:185], v[168:171], v[130:133], v[2:5]
	v_mfma_f32_16x16x32_f16 v[2:5], v[138:141], v[216:219], v[42:45]
	v_mfma_f32_16x16x32_f16 v[150:153], v[168:171], v[224:227], v[2:5]
	v_mfma_f32_16x16x32_f16 v[2:5], v[174:177], v[110:113], v[54:57]
	v_mfma_f32_16x16x32_f16 v[178:181], v[228:231], v[130:133], v[2:5]
	v_mfma_f32_16x16x32_f16 v[2:5], v[174:177], v[216:219], v[66:69]
	v_mfma_f32_16x16x32_f16 v[146:149], v[228:231], v[224:227], v[2:5]
	s_barrier
	s_nop 4
	ds_read_b128 v[2:5], v142
	ds_read_b128 v[6:9], v143
	ds_read_b128 v[10:13], v144
	ds_read_b128 v[18:21], v145
	s_waitcnt vmcnt(0)
	s_barrier
	s_waitcnt lgkmcnt(0)
	v_mfma_f32_16x16x32_f16 v[14:17], v[78:81], v[2:5], v[14:17]
	v_mfma_f32_16x16x32_f16 v[126:129], v[114:117], v[6:9], v[14:17]
	v_mfma_f32_16x16x32_f16 v[14:17], v[78:81], v[10:13], v[22:25]
	v_mfma_f32_16x16x32_f16 v[78:81], v[114:117], v[18:21], v[14:17]
	v_mfma_f32_16x16x32_f16 v[14:17], v[118:121], v[2:5], v[34:37]
	v_mfma_f32_16x16x32_f16 v[122:125], v[134:137], v[6:9], v[14:17]
	v_mfma_f32_16x16x32_f16 v[14:17], v[118:121], v[10:13], v[46:49]
	v_mfma_f32_16x16x32_f16 v[66:69], v[134:137], v[18:21], v[14:17]
	v_mfma_f32_16x16x32_f16 v[14:17], v[138:141], v[2:5], v[58:61]
	v_mfma_f32_16x16x32_f16 v[118:121], v[168:171], v[6:9], v[14:17]
	v_mfma_f32_16x16x32_f16 v[14:17], v[138:141], v[10:13], v[70:73]
	v_mfma_f32_16x16x32_f16 v[54:57], v[168:171], v[18:21], v[14:17]
	v_mfma_f32_16x16x32_f16 v[14:17], v[174:177], v[2:5], v[164:167]
	v_mfma_f32_16x16x32_f16 v[114:117], v[228:231], v[6:9], v[14:17]
	v_mfma_f32_16x16x32_f16 v[14:17], v[174:177], v[10:13], v[86:89]
	v_mfma_f32_16x16x32_f16 v[42:45], v[228:231], v[18:21], v[14:17]
	s_barrier
	s_nop 4
	ds_read_b128 v[14:17], v173 offset:49152
	ds_read_b128 v[22:25], v173 offset:50176
	ds_read_b128 v[30:33], v173 offset:51200
	ds_read_b128 v[34:37], v173 offset:52224
	ds_read_b128 v[46:49], v173 offset:53248
	ds_read_b128 v[58:61], v173 offset:54272
	ds_read_b128 v[70:73], v173 offset:55296
	ds_read_b128 v[86:89], v173 offset:56320
	s_barrier
	s_waitcnt lgkmcnt(0)
	v_mfma_f32_16x16x32_f16 v[26:29], v[14:17], v[110:113], v[26:29]
	v_mfma_f32_16x16x32_f16 v[174:177], v[22:25], v[130:133], v[26:29]
	v_mfma_f32_16x16x32_f16 v[26:29], v[14:17], v[216:219], v[38:41]
	v_mfma_f32_16x16x32_f16 v[142:145], v[22:25], v[224:227], v[26:29]
	v_mfma_f32_16x16x32_f16 v[26:29], v[30:33], v[110:113], v[50:53]
	v_mfma_f32_16x16x32_f16 v[170:173], v[34:37], v[130:133], v[26:29]
	v_mfma_f32_16x16x32_f16 v[26:29], v[30:33], v[216:219], v[62:65]
	v_mfma_f32_16x16x32_f16 v[138:141], v[34:37], v[224:227], v[26:29]
	v_mfma_f32_16x16x32_f16 v[26:29], v[46:49], v[110:113], v[74:77]
	v_mfma_f32_16x16x32_f16 v[166:169], v[58:61], v[130:133], v[26:29]
	v_mfma_f32_16x16x32_f16 v[26:29], v[46:49], v[216:219], v[82:85]
	v_mfma_f32_16x16x32_f16 v[134:137], v[58:61], v[224:227], v[26:29]
	v_mfma_f32_16x16x32_f16 v[26:29], v[70:73], v[110:113], v[90:93]
	v_mfma_f32_16x16x32_f16 v[162:165], v[86:89], v[130:133], v[26:29]
	v_mfma_f32_16x16x32_f16 v[26:29], v[70:73], v[216:219], v[94:97]
	v_mfma_f32_16x16x32_f16 v[130:133], v[86:89], v[224:227], v[26:29]
	v_mfma_f32_16x16x32_f16 v[26:29], v[14:17], v[2:5], v[98:101]
	v_mfma_f32_16x16x32_f16 v[14:17], v[14:17], v[10:13], v[102:105]
	v_mfma_f32_16x16x32_f16 v[38:41], v[22:25], v[18:21], v[14:17]
	v_mfma_f32_16x16x32_f16 v[14:17], v[30:33], v[2:5], v[106:109]
	v_mfma_f32_16x16x32_f16 v[106:109], v[34:37], v[6:9], v[14:17]
	v_mfma_f32_16x16x32_f16 v[14:17], v[30:33], v[10:13], v[200:203]
	v_mfma_f32_16x16x32_f16 v[110:113], v[22:25], v[6:9], v[26:29]
	v_mfma_f32_16x16x32_f16 v[26:29], v[34:37], v[18:21], v[14:17]
	v_mfma_f32_16x16x32_f16 v[14:17], v[46:49], v[2:5], v[204:207]
	v_mfma_f32_16x16x32_f16 v[2:5], v[70:73], v[2:5], v[212:215]
	v_mfma_f32_16x16x32_f16 v[102:105], v[58:61], v[6:9], v[14:17]
	v_mfma_f32_16x16x32_f16 v[14:17], v[46:49], v[10:13], v[220:223]
	v_mfma_f32_16x16x32_f16 v[98:101], v[86:89], v[6:9], v[2:5]
	v_mfma_f32_16x16x32_f16 v[2:5], v[70:73], v[10:13], v[196:199]
	v_mfma_f32_16x16x32_f16 v[14:17], v[58:61], v[18:21], v[14:17]
	v_mfma_f32_16x16x32_f16 v[2:5], v[86:89], v[18:21], v[2:5]
	s_cmpk_gt_u32 s65, 0xff
	s_barrier
	s_cbranch_scc1 .LBB7_242
	s_barrier

.LBB8_41:
	ds_read_b128 v[182:185], v171
	ds_read_b128 v[186:189], v173
	ds_read_b128 v[190:193], v174
	ds_read_b128 v[194:197], v175
	v_add_u32_e32 v177, 0xc000, v148
	v_lshl_add_u64 v[246:247], v[134:135], 0, s[44:45]
	v_add_u32_e32 v176, s48, v170
	v_lshl_add_u64 v[178:179], v[246:247], 0, s[28:29]
	s_mov_b32 m0, s75
	ds_read_b128 v[198:201], v176
	ds_read_b128 v[202:205], v176 offset:1024
	ds_read_b128 v[206:209], v176 offset:2048
	ds_read_b128 v[210:213], v176 offset:3072
	ds_read_b128 v[214:217], v176 offset:4096
	ds_read_b128 v[218:221], v176 offset:5120
	ds_read_b128 v[222:225], v176 offset:6144
	ds_read_b128 v[226:229], v176 offset:7168
	global_load_lds_dwordx4 v[178:179], off
	v_add_u32_e32 v178, 0xe000, v148
	v_lshl_add_u64 v[248:249], v[136:137], 0, s[44:45]
	s_mov_b32 m0, s76
	v_lshl_add_u64 v[230:231], v[248:249], 0, s[28:29]
	global_load_lds_dwordx4 v[230:231], off
	s_waitcnt lgkmcnt(8)
	s_barrier
	s_waitcnt lgkmcnt(0)
	v_mfma_f32_16x16x32_f16 v[126:129], v[198:201], v[182:185], v[126:129]
	v_mfma_f32_16x16x32_f16 v[122:125], v[198:201], v[190:193], v[122:125]
	v_mfma_f32_16x16x32_f16 v[118:121], v[206:209], v[182:185], v[118:121]
	v_mfma_f32_16x16x32_f16 v[114:117], v[206:209], v[190:193], v[114:117]
	v_mfma_f32_16x16x32_f16 v[110:113], v[214:217], v[182:185], v[110:113]
	v_mfma_f32_16x16x32_f16 v[106:109], v[214:217], v[190:193], v[106:109]
	v_mfma_f32_16x16x32_f16 v[102:105], v[222:225], v[182:185], v[102:105]
	v_mfma_f32_16x16x32_f16 v[98:101], v[222:225], v[190:193], v[98:101]
	v_mfma_f32_16x16x32_f16 v[126:129], v[202:205], v[186:189], v[126:129]
	v_mfma_f32_16x16x32_f16 v[122:125], v[202:205], v[194:197], v[122:125]
	v_mfma_f32_16x16x32_f16 v[118:121], v[210:213], v[186:189], v[118:121]
	v_mfma_f32_16x16x32_f16 v[114:117], v[210:213], v[194:197], v[114:117]
	v_mfma_f32_16x16x32_f16 v[110:113], v[218:221], v[186:189], v[110:113]
	v_mfma_f32_16x16x32_f16 v[106:109], v[218:221], v[194:197], v[106:109]
	v_mfma_f32_16x16x32_f16 v[102:105], v[226:229], v[186:189], v[102:105]
	v_mfma_f32_16x16x32_f16 v[98:101], v[226:229], v[194:197], v[98:101]
	s_barrier
	v_lshl_add_u64 v[250:251], v[138:139], 0, s[44:45]
	v_lshl_add_u64 v[252:253], v[250:251], 0, s[30:31]
	s_mov_b32 m0, s77
	ds_read_b128 v[230:233], v162
	ds_read_b128 v[234:237], v163
	ds_read_b128 v[238:241], v164
	ds_read_b128 v[242:245], v165
	global_load_lds_dwordx4 v[252:253], off
	v_lshl_add_u64 v[252:253], v[140:141], 0, s[44:45]
	s_mov_b32 m0, s78
	v_lshl_add_u64 v[254:255], v[252:253], 0, s[30:31]
	global_load_lds_dwordx4 v[254:255], off
	s_barrier
	s_waitcnt lgkmcnt(0)
	v_mfma_f32_16x16x32_f16 v[94:97], v[198:201], v[230:233], v[94:97]
	v_mfma_f32_16x16x32_f16 v[90:93], v[198:201], v[238:241], v[90:93]
	v_mfma_f32_16x16x32_f16 v[86:89], v[206:209], v[230:233], v[86:89]
	v_mfma_f32_16x16x32_f16 v[82:85], v[206:209], v[238:241], v[82:85]
	v_mfma_f32_16x16x32_f16 v[78:81], v[214:217], v[230:233], v[78:81]
	v_mfma_f32_16x16x32_f16 v[74:77], v[214:217], v[238:241], v[74:77]
	v_mfma_f32_16x16x32_f16 v[70:73], v[222:225], v[230:233], v[70:73]
	v_mfma_f32_16x16x32_f16 v[66:69], v[222:225], v[238:241], v[66:69]
	v_mfma_f32_16x16x32_f16 v[94:97], v[202:205], v[234:237], v[94:97]
	v_mfma_f32_16x16x32_f16 v[90:93], v[202:205], v[242:245], v[90:93]
	v_mfma_f32_16x16x32_f16 v[86:89], v[210:213], v[234:237], v[86:89]
	v_mfma_f32_16x16x32_f16 v[82:85], v[210:213], v[242:245], v[82:85]
	v_mfma_f32_16x16x32_f16 v[78:81], v[218:221], v[234:237], v[78:81]
	v_mfma_f32_16x16x32_f16 v[74:77], v[218:221], v[242:245], v[74:77]
	v_mfma_f32_16x16x32_f16 v[70:73], v[226:229], v[234:237], v[70:73]
	v_mfma_f32_16x16x32_f16 v[66:69], v[226:229], v[242:245], v[66:69]
	v_lshl_add_u64 v[254:255], v[246:247], 0, s[30:31]
	s_mov_b32 m0, s79
	s_barrier
	ds_read_b128 v[198:201], v176 offset:16384
	ds_read_b128 v[202:205], v176 offset:17408
	ds_read_b128 v[206:209], v176 offset:18432
	ds_read_b128 v[210:213], v176 offset:19456
	ds_read_b128 v[214:217], v176 offset:20480
	ds_read_b128 v[218:221], v176 offset:21504
	ds_read_b128 v[222:225], v176 offset:22528
	ds_read_b128 v[226:229], v176 offset:23552
	global_load_lds_dwordx4 v[254:255], off
	s_mov_b32 m0, s80
	v_lshl_add_u64 v[254:255], v[248:249], 0, s[30:31]
	global_load_lds_dwordx4 v[254:255], off
	s_barrier
	s_waitcnt lgkmcnt(0)
	v_mfma_f32_16x16x32_f16 v[62:65], v[198:201], v[182:185], v[62:65]
	v_mfma_f32_16x16x32_f16 v[58:61], v[198:201], v[190:193], v[58:61]
	v_mfma_f32_16x16x32_f16 v[54:57], v[206:209], v[182:185], v[54:57]
	v_mfma_f32_16x16x32_f16 v[50:53], v[206:209], v[190:193], v[50:53]
	v_mfma_f32_16x16x32_f16 v[46:49], v[214:217], v[182:185], v[46:49]
	v_mfma_f32_16x16x32_f16 v[42:45], v[214:217], v[190:193], v[42:45]
	v_mfma_f32_16x16x32_f16 v[38:41], v[222:225], v[182:185], v[38:41]
	v_mfma_f32_16x16x32_f16 v[34:37], v[222:225], v[190:193], v[34:37]
	v_mfma_f32_16x16x32_f16 v[62:65], v[202:205], v[186:189], v[62:65]
	v_mfma_f32_16x16x32_f16 v[58:61], v[202:205], v[194:197], v[58:61]
	v_mfma_f32_16x16x32_f16 v[54:57], v[210:213], v[186:189], v[54:57]
	v_mfma_f32_16x16x32_f16 v[50:53], v[210:213], v[194:197], v[50:53]
	v_mfma_f32_16x16x32_f16 v[46:49], v[218:221], v[186:189], v[46:49]
	v_mfma_f32_16x16x32_f16 v[42:45], v[218:221], v[194:197], v[42:45]
	v_mfma_f32_16x16x32_f16 v[38:41], v[226:229], v[186:189], v[38:41]
	v_mfma_f32_16x16x32_f16 v[34:37], v[226:229], v[194:197], v[34:37]
	s_barrier
	s_mov_b32 m0, s81
	v_lshl_add_u64 v[182:183], v[250:251], 0, s[34:35]
	global_load_lds_dwordx4 v[182:183], off
	s_mov_b32 m0, s82
	v_lshl_add_u64 v[182:183], v[252:253], 0, s[34:35]
	global_load_lds_dwordx4 v[182:183], off
	s_waitcnt vmcnt(6)
	s_barrier
	v_mfma_f32_16x16x32_f16 v[30:33], v[198:201], v[230:233], v[30:33]
	v_mfma_f32_16x16x32_f16 v[26:29], v[198:201], v[238:241], v[26:29]
	v_mfma_f32_16x16x32_f16 v[22:25], v[206:209], v[230:233], v[22:25]
	v_mfma_f32_16x16x32_f16 v[18:21], v[206:209], v[238:241], v[18:21]
	v_mfma_f32_16x16x32_f16 v[14:17], v[214:217], v[230:233], v[14:17]
	v_mfma_f32_16x16x32_f16 v[10:13], v[214:217], v[238:241], v[10:13]
	v_mfma_f32_16x16x32_f16 v[6:9], v[222:225], v[230:233], v[6:9]
	v_mfma_f32_16x16x32_f16 v[2:5], v[222:225], v[238:241], v[2:5]
	v_mfma_f32_16x16x32_f16 v[30:33], v[202:205], v[234:237], v[30:33]
	v_mfma_f32_16x16x32_f16 v[26:29], v[202:205], v[242:245], v[26:29]
	v_mfma_f32_16x16x32_f16 v[22:25], v[210:213], v[234:237], v[22:25]
	v_mfma_f32_16x16x32_f16 v[18:21], v[210:213], v[242:245], v[18:21]
	v_mfma_f32_16x16x32_f16 v[14:17], v[218:221], v[234:237], v[14:17]
	v_mfma_f32_16x16x32_f16 v[10:13], v[218:221], v[242:245], v[10:13]
	v_mfma_f32_16x16x32_f16 v[6:9], v[226:229], v[234:237], v[6:9]
	v_mfma_f32_16x16x32_f16 v[2:5], v[226:229], v[242:245], v[2:5]
	s_barrier
	ds_read_b128 v[182:185], v144
	ds_read_b128 v[186:189], v145
	ds_read_b128 v[190:193], v146
	ds_read_b128 v[194:197], v147
	v_lshl_add_u64 v[230:231], v[246:247], 0, s[34:35]
	s_mov_b32 m0, s83
	ds_read_b128 v[198:201], v176 offset:32768
	ds_read_b128 v[202:205], v176 offset:33792
	ds_read_b128 v[206:209], v176 offset:34816
	ds_read_b128 v[210:213], v176 offset:35840
	ds_read_b128 v[214:217], v176 offset:36864
	ds_read_b128 v[218:221], v176 offset:37888
	ds_read_b128 v[222:225], v176 offset:38912
	ds_read_b128 v[226:229], v176 offset:39936
	global_load_lds_dwordx4 v[230:231], off
	s_mov_b32 m0, s84
	v_lshl_add_u64 v[230:231], v[248:249], 0, s[34:35]
	global_load_lds_dwordx4 v[230:231], off
	s_waitcnt lgkmcnt(8)
	s_barrier
	s_waitcnt lgkmcnt(0)
	v_mfma_f32_16x16x32_f16 v[126:129], v[198:201], v[182:185], v[126:129]
	v_mfma_f32_16x16x32_f16 v[122:125], v[198:201], v[190:193], v[122:125]
	v_mfma_f32_16x16x32_f16 v[118:121], v[206:209], v[182:185], v[118:121]
	v_mfma_f32_16x16x32_f16 v[114:117], v[206:209], v[190:193], v[114:117]
	v_mfma_f32_16x16x32_f16 v[110:113], v[214:217], v[182:185], v[110:113]
	v_mfma_f32_16x16x32_f16 v[106:109], v[214:217], v[190:193], v[106:109]
	v_mfma_f32_16x16x32_f16 v[102:105], v[222:225], v[182:185], v[102:105]
	v_mfma_f32_16x16x32_f16 v[98:101], v[222:225], v[190:193], v[98:101]
	v_mfma_f32_16x16x32_f16 v[126:129], v[202:205], v[186:189], v[126:129]
	v_mfma_f32_16x16x32_f16 v[122:125], v[202:205], v[194:197], v[122:125]
	v_mfma_f32_16x16x32_f16 v[118:121], v[210:213], v[186:189], v[118:121]
	v_mfma_f32_16x16x32_f16 v[114:117], v[210:213], v[194:197], v[114:117]
	v_mfma_f32_16x16x32_f16 v[110:113], v[218:221], v[186:189], v[110:113]
	v_mfma_f32_16x16x32_f16 v[106:109], v[218:221], v[194:197], v[106:109]
	v_mfma_f32_16x16x32_f16 v[102:105], v[226:229], v[186:189], v[102:105]
	v_mfma_f32_16x16x32_f16 v[98:101], v[226:229], v[194:197], v[98:101]
	s_barrier
	v_lshl_add_u64 v[254:255], v[250:251], 0, s[36:37]
	s_mov_b32 m0, s85
	ds_read_b128 v[230:233], v150
	ds_read_b128 v[234:237], v151
	ds_read_b128 v[238:241], v152
	ds_read_b128 v[242:245], v153
	global_load_lds_dwordx4 v[254:255], off
	s_mov_b32 m0, s86
	v_lshl_add_u64 v[254:255], v[252:253], 0, s[36:37]
	global_load_lds_dwordx4 v[254:255], off
	s_barrier
	s_waitcnt lgkmcnt(0)
	v_mfma_f32_16x16x32_f16 v[94:97], v[198:201], v[230:233], v[94:97]
	v_mfma_f32_16x16x32_f16 v[90:93], v[198:201], v[238:241], v[90:93]
	v_mfma_f32_16x16x32_f16 v[86:89], v[206:209], v[230:233], v[86:89]
	v_mfma_f32_16x16x32_f16 v[82:85], v[206:209], v[238:241], v[82:85]
	v_mfma_f32_16x16x32_f16 v[78:81], v[214:217], v[230:233], v[78:81]
	v_mfma_f32_16x16x32_f16 v[74:77], v[214:217], v[238:241], v[74:77]
	v_mfma_f32_16x16x32_f16 v[70:73], v[222:225], v[230:233], v[70:73]
	v_mfma_f32_16x16x32_f16 v[66:69], v[222:225], v[238:241], v[66:69]
	v_mfma_f32_16x16x32_f16 v[94:97], v[202:205], v[234:237], v[94:97]
	v_mfma_f32_16x16x32_f16 v[90:93], v[202:205], v[242:245], v[90:93]
	v_mfma_f32_16x16x32_f16 v[86:89], v[210:213], v[234:237], v[86:89]
	v_mfma_f32_16x16x32_f16 v[82:85], v[210:213], v[242:245], v[82:85]
	v_mfma_f32_16x16x32_f16 v[78:81], v[218:221], v[234:237], v[78:81]
	v_mfma_f32_16x16x32_f16 v[74:77], v[218:221], v[242:245], v[74:77]
	v_mfma_f32_16x16x32_f16 v[70:73], v[226:229], v[234:237], v[70:73]
	v_mfma_f32_16x16x32_f16 v[66:69], v[226:229], v[242:245], v[66:69]
	v_lshl_add_u64 v[246:247], v[246:247], 0, s[36:37]
	s_mov_b32 m0, s87
	s_barrier
	ds_read_b128 v[198:201], v176 offset:49152
	ds_read_b128 v[202:205], v176 offset:50176
	ds_read_b128 v[206:209], v176 offset:51200
	ds_read_b128 v[210:213], v176 offset:52224
	ds_read_b128 v[214:217], v176 offset:53248
	ds_read_b128 v[218:221], v176 offset:54272
	ds_read_b128 v[222:225], v176 offset:55296
	ds_read_b128 v[226:229], v176 offset:56320
	global_load_lds_dwordx4 v[246:247], off
	s_mov_b32 m0, s88
	v_lshl_add_u64 v[246:247], v[248:249], 0, s[36:37]
	global_load_lds_dwordx4 v[246:247], off
	s_barrier
	s_waitcnt lgkmcnt(0)
	v_mfma_f32_16x16x32_f16 v[62:65], v[198:201], v[182:185], v[62:65]
	v_mfma_f32_16x16x32_f16 v[58:61], v[198:201], v[190:193], v[58:61]
	v_mfma_f32_16x16x32_f16 v[54:57], v[206:209], v[182:185], v[54:57]
	v_mfma_f32_16x16x32_f16 v[50:53], v[206:209], v[190:193], v[50:53]
	v_mfma_f32_16x16x32_f16 v[46:49], v[214:217], v[182:185], v[46:49]
	v_mfma_f32_16x16x32_f16 v[42:45], v[214:217], v[190:193], v[42:45]
	v_mfma_f32_16x16x32_f16 v[38:41], v[222:225], v[182:185], v[38:41]
	v_mfma_f32_16x16x32_f16 v[34:37], v[222:225], v[190:193], v[34:37]
	v_mfma_f32_16x16x32_f16 v[62:65], v[202:205], v[186:189], v[62:65]
	v_mfma_f32_16x16x32_f16 v[58:61], v[202:205], v[194:197], v[58:61]
	v_mfma_f32_16x16x32_f16 v[54:57], v[210:213], v[186:189], v[54:57]
	v_mfma_f32_16x16x32_f16 v[50:53], v[210:213], v[194:197], v[50:53]
	v_mfma_f32_16x16x32_f16 v[46:49], v[218:221], v[186:189], v[46:49]
	v_mfma_f32_16x16x32_f16 v[42:45], v[218:221], v[194:197], v[42:45]
	v_mfma_f32_16x16x32_f16 v[38:41], v[226:229], v[186:189], v[38:41]
	v_mfma_f32_16x16x32_f16 v[34:37], v[226:229], v[194:197], v[34:37]
	s_barrier
	s_mov_b32 m0, s89
	v_lshl_add_u64 v[182:183], v[250:251], 0, s[38:39]
	global_load_lds_dwordx4 v[182:183], off
	s_mov_b32 m0, s90
	v_lshl_add_u64 v[182:183], v[252:253], 0, s[38:39]
	global_load_lds_dwordx4 v[182:183], off
	s_waitcnt vmcnt(6)
	s_barrier
	v_mfma_f32_16x16x32_f16 v[30:33], v[198:201], v[230:233], v[30:33]
	v_mfma_f32_16x16x32_f16 v[26:29], v[198:201], v[238:241], v[26:29]
	v_mfma_f32_16x16x32_f16 v[22:25], v[206:209], v[230:233], v[22:25]
	v_mfma_f32_16x16x32_f16 v[18:21], v[206:209], v[238:241], v[18:21]
	v_mfma_f32_16x16x32_f16 v[14:17], v[214:217], v[230:233], v[14:17]
	v_mfma_f32_16x16x32_f16 v[10:13], v[214:217], v[238:241], v[10:13]
	v_mfma_f32_16x16x32_f16 v[6:9], v[222:225], v[230:233], v[6:9]
	v_mfma_f32_16x16x32_f16 v[2:5], v[222:225], v[238:241], v[2:5]
	v_mfma_f32_16x16x32_f16 v[30:33], v[202:205], v[234:237], v[30:33]
	v_mfma_f32_16x16x32_f16 v[26:29], v[202:205], v[242:245], v[26:29]
	v_mfma_f32_16x16x32_f16 v[22:25], v[210:213], v[234:237], v[22:25]
	v_mfma_f32_16x16x32_f16 v[18:21], v[210:213], v[242:245], v[18:21]
	v_mfma_f32_16x16x32_f16 v[14:17], v[218:221], v[234:237], v[14:17]
	v_mfma_f32_16x16x32_f16 v[10:13], v[218:221], v[242:245], v[10:13]
	v_mfma_f32_16x16x32_f16 v[6:9], v[226:229], v[234:237], v[6:9]
	v_mfma_f32_16x16x32_f16 v[2:5], v[226:229], v[242:245], v[2:5]
	s_add_i32 s46, s46, 2
	s_add_u32 s44, s44, 0x100
	s_addc_u32 s45, s45, 0
	s_cmp_lt_u32 s46, 4
	s_barrier
	s_cbranch_scc1 .LBB8_41
	s_add_u32 s42, s42, 0x20380
	s_addc_u32 s43, s43, 0
	v_readfirstlane_b32 s44, v177
	v_lshl_add_u64 v[130:131], v[130:131], 1, s[42:43]
	s_mov_b32 m0, s44
	ds_read_b128 v[134:137], v171
	ds_read_b128 v[138:141], v173
	ds_read_b128 v[154:157], v174
	ds_read_b128 v[168:171], v175
	ds_read_b128 v[182:185], v176
	ds_read_b128 v[186:189], v176 offset:1024
	ds_read_b128 v[190:193], v176 offset:2048
	ds_read_b128 v[194:197], v176 offset:3072
	ds_read_b128 v[198:201], v176 offset:4096
	ds_read_b128 v[202:205], v176 offset:5120
	ds_read_b128 v[206:209], v176 offset:6144
	ds_read_b128 v[210:213], v176 offset:7168
	global_load_lds_dwordx4 v[130:131], off
	v_lshl_add_u64 v[130:131], v[132:133], 1, s[42:43]
	v_readfirstlane_b32 s42, v178
	s_mov_b32 m0, s42
	s_nop 0
	global_load_lds_dwordx4 v[130:131], off
	s_barrier
	s_waitcnt lgkmcnt(0)
	v_mfma_f32_16x16x32_f16 v[122:125], v[182:185], v[154:157], v[122:125]
	v_mfma_f32_16x16x32_f16 v[110:113], v[198:201], v[134:137], v[110:113]
	v_mfma_f32_16x16x32_f16 v[98:101], v[206:209], v[154:157], v[98:101]
	v_mfma_f32_16x16x32_f16 v[126:129], v[182:185], v[134:137], v[126:129]
	v_mfma_f32_16x16x32_f16 v[122:125], v[186:189], v[168:171], v[122:125]
	v_mfma_f32_16x16x32_f16 v[118:121], v[190:193], v[134:137], v[118:121]
	v_mfma_f32_16x16x32_f16 v[114:117], v[190:193], v[154:157], v[114:117]
	v_mfma_f32_16x16x32_f16 v[130:133], v[202:205], v[138:141], v[110:113]
	v_mfma_f32_16x16x32_f16 v[106:109], v[198:201], v[154:157], v[106:109]
	v_mfma_f32_16x16x32_f16 v[102:105], v[206:209], v[134:137], v[102:105]
	v_mfma_f32_16x16x32_f16 v[98:101], v[210:213], v[168:171], v[98:101]
	v_mfma_f32_16x16x32_f16 v[126:129], v[186:189], v[138:141], v[126:129]
	v_mfma_f32_16x16x32_f16 v[118:121], v[194:197], v[138:141], v[118:121]
	v_mfma_f32_16x16x32_f16 v[114:117], v[194:197], v[168:171], v[114:117]
	v_mfma_f32_16x16x32_f16 v[214:217], v[202:205], v[168:171], v[106:109]
	v_mfma_f32_16x16x32_f16 v[102:105], v[210:213], v[138:141], v[102:105]
	s_barrier
	ds_read_b128 v[106:109], v162
	ds_read_b128 v[110:113], v163
	ds_read_b128 v[160:163], v164
	ds_read_b128 v[218:221], v165
	s_barrier
	s_waitcnt lgkmcnt(0)
	v_mfma_f32_16x16x32_f16 v[82:85], v[190:193], v[160:163], v[82:85]
	v_mfma_f32_16x16x32_f16 v[78:81], v[198:201], v[106:109], v[78:81]
	v_mfma_f32_16x16x32_f16 v[74:77], v[198:201], v[160:163], v[74:77]
	v_mfma_f32_16x16x32_f16 v[70:73], v[206:209], v[106:109], v[70:73]
	v_mfma_f32_16x16x32_f16 v[66:69], v[206:209], v[160:163], v[66:69]
	v_mfma_f32_16x16x32_f16 v[94:97], v[182:185], v[106:109], v[94:97]
	v_mfma_f32_16x16x32_f16 v[90:93], v[182:185], v[160:163], v[90:93]
	v_mfma_f32_16x16x32_f16 v[86:89], v[190:193], v[106:109], v[86:89]
	v_mfma_f32_16x16x32_f16 v[82:85], v[194:197], v[218:221], v[82:85]
	v_mfma_f32_16x16x32_f16 v[78:81], v[202:205], v[110:113], v[78:81]
	v_mfma_f32_16x16x32_f16 v[74:77], v[202:205], v[218:221], v[74:77]
	v_mfma_f32_16x16x32_f16 v[70:73], v[210:213], v[110:113], v[70:73]
	v_mfma_f32_16x16x32_f16 v[66:69], v[210:213], v[218:221], v[66:69]
	v_mfma_f32_16x16x32_f16 v[222:225], v[186:189], v[110:113], v[94:97]
	v_mfma_f32_16x16x32_f16 v[182:185], v[186:189], v[218:221], v[90:93]
	v_mfma_f32_16x16x32_f16 v[86:89], v[194:197], v[110:113], v[86:89]
	s_barrier
	ds_read_b128 v[90:93], v176 offset:16384
	ds_read_b128 v[94:97], v176 offset:17408
	ds_read_b128 v[186:189], v176 offset:18432
	ds_read_b128 v[190:193], v176 offset:19456
	ds_read_b128 v[194:197], v176 offset:20480
	ds_read_b128 v[198:201], v176 offset:21504
	ds_read_b128 v[202:205], v176 offset:22528
	ds_read_b128 v[206:209], v176 offset:23552
	s_waitcnt vmcnt(4)
	s_barrier
	s_waitcnt lgkmcnt(0)
	v_mfma_f32_16x16x32_f16 v[46:49], v[194:197], v[134:137], v[46:49]
	v_mfma_f32_16x16x32_f16 v[42:45], v[194:197], v[154:157], v[42:45]
	v_mfma_f32_16x16x32_f16 v[38:41], v[202:205], v[134:137], v[38:41]
	v_mfma_f32_16x16x32_f16 v[34:37], v[202:205], v[154:157], v[34:37]
	v_mfma_f32_16x16x32_f16 v[62:65], v[90:93], v[134:137], v[62:65]
	v_mfma_f32_16x16x32_f16 v[58:61], v[90:93], v[154:157], v[58:61]
	v_mfma_f32_16x16x32_f16 v[54:57], v[186:189], v[134:137], v[54:57]
	v_mfma_f32_16x16x32_f16 v[50:53], v[186:189], v[154:157], v[50:53]
	v_mfma_f32_16x16x32_f16 v[46:49], v[198:201], v[138:141], v[46:49]
	v_mfma_f32_16x16x32_f16 v[42:45], v[198:201], v[168:171], v[42:45]
	v_mfma_f32_16x16x32_f16 v[38:41], v[206:209], v[138:141], v[38:41]
	v_mfma_f32_16x16x32_f16 v[34:37], v[206:209], v[168:171], v[34:37]
	v_mfma_f32_16x16x32_f16 v[210:213], v[94:97], v[138:141], v[62:65]
	v_mfma_f32_16x16x32_f16 v[226:229], v[94:97], v[168:171], v[58:61]
	v_mfma_f32_16x16x32_f16 v[230:233], v[190:193], v[138:141], v[54:57]
	v_mfma_f32_16x16x32_f16 v[234:237], v[190:193], v[168:171], v[50:53]
	v_mfma_f32_16x16x32_f16 v[2:5], v[202:205], v[160:163], v[2:5]
	v_mfma_f32_16x16x32_f16 v[30:33], v[90:93], v[106:109], v[30:33]
	v_mfma_f32_16x16x32_f16 v[26:29], v[90:93], v[160:163], v[26:29]
	v_mfma_f32_16x16x32_f16 v[22:25], v[186:189], v[106:109], v[22:25]
	v_mfma_f32_16x16x32_f16 v[18:21], v[186:189], v[160:163], v[18:21]
	v_mfma_f32_16x16x32_f16 v[14:17], v[194:197], v[106:109], v[14:17]
	v_mfma_f32_16x16x32_f16 v[10:13], v[194:197], v[160:163], v[10:13]
	v_mfma_f32_16x16x32_f16 v[6:9], v[202:205], v[106:109], v[6:9]
	v_mfma_f32_16x16x32_f16 v[2:5], v[206:209], v[218:221], v[2:5]
	v_mfma_f32_16x16x32_f16 v[138:141], v[94:97], v[110:113], v[30:33]
	v_mfma_f32_16x16x32_f16 v[168:171], v[94:97], v[218:221], v[26:29]
	v_mfma_f32_16x16x32_f16 v[238:241], v[190:193], v[110:113], v[22:25]
	v_mfma_f32_16x16x32_f16 v[186:189], v[190:193], v[218:221], v[18:21]
	v_mfma_f32_16x16x32_f16 v[190:193], v[198:201], v[110:113], v[14:17]
	v_mfma_f32_16x16x32_f16 v[194:197], v[198:201], v[218:221], v[10:13]
	v_mfma_f32_16x16x32_f16 v[198:201], v[206:209], v[110:113], v[6:9]
	s_barrier
	s_nop 0
	ds_read_b128 v[6:9], v144
	ds_read_b128 v[10:13], v145
	ds_read_b128 v[14:17], v146
	ds_read_b128 v[160:163], v147
	ds_read_b128 v[18:21], v176 offset:32768
	ds_read_b128 v[22:25], v176 offset:33792
	ds_read_b128 v[26:29], v176 offset:34816
	ds_read_b128 v[50:53], v176 offset:35840
	ds_read_b128 v[202:205], v176 offset:36864
	ds_read_b128 v[206:209], v176 offset:37888
	ds_read_b128 v[218:221], v176 offset:38912
	ds_read_b128 v[242:245], v176 offset:39936
	s_waitcnt vmcnt(2)
	s_barrier
	s_waitcnt lgkmcnt(0)
	v_mfma_f32_16x16x32_f16 v[30:33], v[18:21], v[6:9], v[126:129]
	v_mfma_f32_16x16x32_f16 v[154:157], v[22:25], v[10:13], v[30:33]
	v_mfma_f32_16x16x32_f16 v[30:33], v[18:21], v[14:17], v[122:125]
	v_mfma_f32_16x16x32_f16 v[110:113], v[22:25], v[160:163], v[30:33]
	v_mfma_f32_16x16x32_f16 v[30:33], v[26:29], v[6:9], v[118:121]
	v_mfma_f32_16x16x32_f16 v[146:149], v[50:53], v[10:13], v[30:33]
	v_mfma_f32_16x16x32_f16 v[30:33], v[26:29], v[14:17], v[114:117]
	v_mfma_f32_16x16x32_f16 v[106:109], v[50:53], v[160:163], v[30:33]
	v_mfma_f32_16x16x32_f16 v[30:33], v[202:205], v[6:9], v[130:133]
	v_mfma_f32_16x16x32_f16 v[142:145], v[206:209], v[10:13], v[30:33]
	v_mfma_f32_16x16x32_f16 v[30:33], v[202:205], v[14:17], v[214:217]
	v_mfma_f32_16x16x32_f16 v[94:97], v[206:209], v[160:163], v[30:33]
	v_mfma_f32_16x16x32_f16 v[30:33], v[218:221], v[6:9], v[102:105]
	v_mfma_f32_16x16x32_f16 v[134:137], v[242:245], v[10:13], v[30:33]
	v_mfma_f32_16x16x32_f16 v[30:33], v[218:221], v[14:17], v[98:101]
	v_mfma_f32_16x16x32_f16 v[90:93], v[242:245], v[160:163], v[30:33]
	s_barrier
	ds_read_b128 v[102:105], v150
	ds_read_b128 v[114:117], v151
	ds_read_b128 v[118:121], v152
	ds_read_b128 v[126:129], v153
	s_waitcnt vmcnt(0)
	s_barrier
	s_waitcnt lgkmcnt(0)
	v_mfma_f32_16x16x32_f16 v[30:33], v[18:21], v[102:105], v[222:225]
	v_mfma_f32_16x16x32_f16 v[18:21], v[18:21], v[118:121], v[182:185]
	v_mfma_f32_16x16x32_f16 v[62:65], v[22:25], v[114:117], v[30:33]
	v_mfma_f32_16x16x32_f16 v[30:33], v[22:25], v[126:129], v[18:21]
	v_mfma_f32_16x16x32_f16 v[18:21], v[26:29], v[102:105], v[86:89]
	v_mfma_f32_16x16x32_f16 v[58:61], v[50:53], v[114:117], v[18:21]
	v_mfma_f32_16x16x32_f16 v[18:21], v[26:29], v[118:121], v[82:85]
	v_mfma_f32_16x16x32_f16 v[26:29], v[50:53], v[126:129], v[18:21]
	v_mfma_f32_16x16x32_f16 v[18:21], v[202:205], v[102:105], v[78:81]
	v_mfma_f32_16x16x32_f16 v[54:57], v[206:209], v[114:117], v[18:21]
	v_mfma_f32_16x16x32_f16 v[18:21], v[202:205], v[118:121], v[74:77]
	v_mfma_f32_16x16x32_f16 v[22:25], v[206:209], v[126:129], v[18:21]
	v_mfma_f32_16x16x32_f16 v[18:21], v[218:221], v[102:105], v[70:73]
	v_mfma_f32_16x16x32_f16 v[50:53], v[242:245], v[114:117], v[18:21]
	v_mfma_f32_16x16x32_f16 v[18:21], v[218:221], v[118:121], v[66:69]
	v_mfma_f32_16x16x32_f16 v[18:21], v[242:245], v[126:129], v[18:21]
	s_barrier
	ds_read_b128 v[86:89], v176 offset:49152
	ds_read_b128 v[150:153], v176 offset:50176
	ds_read_b128 v[182:185], v176 offset:51200
	ds_read_b128 v[202:205], v176 offset:52224
	ds_read_b128 v[206:209], v176 offset:53248
	ds_read_b128 v[214:217], v176 offset:54272
	ds_read_b128 v[218:221], v176 offset:55296
	ds_read_b128 v[174:177], v176 offset:56320
	s_barrier
	s_waitcnt lgkmcnt(0)
	v_mfma_f32_16x16x32_f16 v[66:69], v[86:89], v[6:9], v[210:213]
	v_mfma_f32_16x16x32_f16 v[130:133], v[150:153], v[10:13], v[66:69]
	v_mfma_f32_16x16x32_f16 v[66:69], v[86:89], v[14:17], v[226:229]
	v_mfma_f32_16x16x32_f16 v[78:81], v[150:153], v[160:163], v[66:69]
	v_mfma_f32_16x16x32_f16 v[66:69], v[182:185], v[6:9], v[230:233]
	v_mfma_f32_16x16x32_f16 v[46:49], v[206:209], v[6:9], v[46:49]
	v_mfma_f32_16x16x32_f16 v[6:9], v[218:221], v[6:9], v[38:41]
	v_mfma_f32_16x16x32_f16 v[122:125], v[202:205], v[10:13], v[66:69]
	v_mfma_f32_16x16x32_f16 v[66:69], v[182:185], v[14:17], v[234:237]
	v_mfma_f32_16x16x32_f16 v[42:45], v[206:209], v[14:17], v[42:45]
	v_mfma_f32_16x16x32_f16 v[82:85], v[174:177], v[10:13], v[6:9]
	v_mfma_f32_16x16x32_f16 v[6:9], v[218:221], v[14:17], v[34:37]
	v_mfma_f32_16x16x32_f16 v[74:77], v[202:205], v[160:163], v[66:69]
	v_mfma_f32_16x16x32_f16 v[98:101], v[214:217], v[10:13], v[46:49]
	v_mfma_f32_16x16x32_f16 v[70:73], v[214:217], v[160:163], v[42:45]
	v_mfma_f32_16x16x32_f16 v[66:69], v[174:177], v[160:163], v[6:9]
	v_mfma_f32_16x16x32_f16 v[6:9], v[86:89], v[102:105], v[138:141]
	v_mfma_f32_16x16x32_f16 v[46:49], v[150:153], v[114:117], v[6:9]
	v_mfma_f32_16x16x32_f16 v[6:9], v[86:89], v[118:121], v[168:171]
	v_mfma_f32_16x16x32_f16 v[14:17], v[150:153], v[126:129], v[6:9]
	v_mfma_f32_16x16x32_f16 v[6:9], v[182:185], v[102:105], v[238:241]
	v_mfma_f32_16x16x32_f16 v[42:45], v[202:205], v[114:117], v[6:9]
	v_mfma_f32_16x16x32_f16 v[6:9], v[182:185], v[118:121], v[186:189]
	v_mfma_f32_16x16x32_f16 v[10:13], v[202:205], v[126:129], v[6:9]
	v_mfma_f32_16x16x32_f16 v[6:9], v[206:209], v[102:105], v[190:193]
	v_mfma_f32_16x16x32_f16 v[38:41], v[214:217], v[114:117], v[6:9]
	v_mfma_f32_16x16x32_f16 v[6:9], v[206:209], v[118:121], v[194:197]
	v_mfma_f32_16x16x32_f16 v[34:37], v[218:221], v[102:105], v[198:201]
	v_mfma_f32_16x16x32_f16 v[2:5], v[218:221], v[118:121], v[2:5]
	v_mfma_f32_16x16x32_f16 v[6:9], v[214:217], v[126:129], v[6:9]
	v_mfma_f32_16x16x32_f16 v[34:37], v[174:177], v[114:117], v[34:37]
	v_mfma_f32_16x16x32_f16 v[2:5], v[174:177], v[126:129], v[2:5]
	s_cmpk_gt_u32 s62, 0xff
	s_barrier
	s_cbranch_scc1 .LBB8_44
	s_barrier

.LBB9_38:
	ds_read_b128 v[176:179], v169
	ds_read_b128 v[180:183], v170
	ds_read_b128 v[184:187], v171
	ds_read_b128 v[188:191], v172
	v_add_u32_e32 v174, 0xc000, v152
	v_lshl_add_u64 v[192:193], v[136:137], 0, s[42:43]
	v_add_u32_e32 v175, 0xe000, v152
	v_add_u32_e32 v173, s39, v168
	v_lshl_add_u64 v[230:231], v[192:193], 0, s[10:11]
	s_mov_b32 m0, s65
	v_lshl_add_u64 v[246:247], v[134:135], 0, s[42:43]
	ds_read_b128 v[198:201], v173
	ds_read_b128 v[202:205], v173 offset:1024
	ds_read_b128 v[206:209], v173 offset:2048
	ds_read_b128 v[210:213], v173 offset:3072
	ds_read_b128 v[214:217], v173 offset:4096
	ds_read_b128 v[218:221], v173 offset:5120
	ds_read_b128 v[222:225], v173 offset:6144
	ds_read_b128 v[226:229], v173 offset:7168
	global_load_lds_dwordx4 v[230:231], off
	s_mov_b32 m0, s66
	v_lshl_add_u64 v[230:231], v[246:247], 0, s[10:11]
	global_load_lds_dwordx4 v[230:231], off
	s_waitcnt lgkmcnt(8)
	s_barrier
	s_waitcnt lgkmcnt(0)
	v_mfma_f32_16x16x32_f16 v[2:5], v[198:201], v[176:179], v[2:5]
	v_mfma_f32_16x16x32_f16 v[6:9], v[198:201], v[184:187], v[6:9]
	v_mfma_f32_16x16x32_f16 v[10:13], v[206:209], v[176:179], v[10:13]
	v_mfma_f32_16x16x32_f16 v[18:21], v[206:209], v[184:187], v[18:21]
	v_mfma_f32_16x16x32_f16 v[30:33], v[214:217], v[176:179], v[30:33]
	v_mfma_f32_16x16x32_f16 v[42:45], v[214:217], v[184:187], v[42:45]
	v_mfma_f32_16x16x32_f16 v[54:57], v[222:225], v[176:179], v[54:57]
	v_mfma_f32_16x16x32_f16 v[66:69], v[222:225], v[184:187], v[66:69]
	v_mfma_f32_16x16x32_f16 v[2:5], v[202:205], v[180:183], v[2:5]
	v_mfma_f32_16x16x32_f16 v[6:9], v[202:205], v[188:191], v[6:9]
	v_mfma_f32_16x16x32_f16 v[10:13], v[210:213], v[180:183], v[10:13]
	v_mfma_f32_16x16x32_f16 v[18:21], v[210:213], v[188:191], v[18:21]
	v_mfma_f32_16x16x32_f16 v[30:33], v[218:221], v[180:183], v[30:33]
	v_mfma_f32_16x16x32_f16 v[42:45], v[218:221], v[188:191], v[42:45]
	v_mfma_f32_16x16x32_f16 v[54:57], v[226:229], v[180:183], v[54:57]
	v_mfma_f32_16x16x32_f16 v[66:69], v[226:229], v[188:191], v[66:69]
	s_barrier
	v_lshl_add_u64 v[248:249], v[140:141], 0, s[42:43]
	v_lshl_add_u64 v[250:251], v[248:249], 0, s[26:27]
	s_mov_b32 m0, s67
	ds_read_b128 v[230:233], v161
	ds_read_b128 v[234:237], v162
	ds_read_b128 v[238:241], v163
	ds_read_b128 v[242:245], v164
	global_load_lds_dwordx4 v[250:251], off
	v_lshl_add_u64 v[250:251], v[138:139], 0, s[42:43]
	s_mov_b32 m0, s68
	v_lshl_add_u64 v[252:253], v[250:251], 0, s[26:27]
	global_load_lds_dwordx4 v[252:253], off
	s_barrier
	s_waitcnt lgkmcnt(0)
	v_mfma_f32_16x16x32_f16 v[14:17], v[198:201], v[230:233], v[14:17]
	v_mfma_f32_16x16x32_f16 v[22:25], v[198:201], v[238:241], v[22:25]
	v_mfma_f32_16x16x32_f16 v[34:37], v[206:209], v[230:233], v[34:37]
	v_mfma_f32_16x16x32_f16 v[46:49], v[206:209], v[238:241], v[46:49]
	v_mfma_f32_16x16x32_f16 v[58:61], v[214:217], v[230:233], v[58:61]
	v_mfma_f32_16x16x32_f16 v[70:73], v[214:217], v[238:241], v[70:73]
	v_mfma_f32_16x16x32_f16 v[78:81], v[222:225], v[230:233], v[78:81]
	v_mfma_f32_16x16x32_f16 v[86:89], v[222:225], v[238:241], v[86:89]
	v_mfma_f32_16x16x32_f16 v[14:17], v[202:205], v[234:237], v[14:17]
	v_mfma_f32_16x16x32_f16 v[22:25], v[202:205], v[242:245], v[22:25]
	v_mfma_f32_16x16x32_f16 v[34:37], v[210:213], v[234:237], v[34:37]
	v_mfma_f32_16x16x32_f16 v[46:49], v[210:213], v[242:245], v[46:49]
	v_mfma_f32_16x16x32_f16 v[58:61], v[218:221], v[234:237], v[58:61]
	v_mfma_f32_16x16x32_f16 v[70:73], v[218:221], v[242:245], v[70:73]
	v_mfma_f32_16x16x32_f16 v[78:81], v[226:229], v[234:237], v[78:81]
	v_mfma_f32_16x16x32_f16 v[86:89], v[226:229], v[242:245], v[86:89]
	v_lshl_add_u64 v[252:253], v[192:193], 0, s[26:27]
	s_mov_b32 m0, s69
	s_barrier
	ds_read_b128 v[198:201], v173 offset:16384
	ds_read_b128 v[202:205], v173 offset:17408
	ds_read_b128 v[206:209], v173 offset:18432
	ds_read_b128 v[210:213], v173 offset:19456
	ds_read_b128 v[214:217], v173 offset:20480
	ds_read_b128 v[218:221], v173 offset:21504
	ds_read_b128 v[222:225], v173 offset:22528
	ds_read_b128 v[226:229], v173 offset:23552
	global_load_lds_dwordx4 v[252:253], off
	s_mov_b32 m0, s70
	v_lshl_add_u64 v[252:253], v[246:247], 0, s[26:27]
	global_load_lds_dwordx4 v[252:253], off
	s_barrier
	s_waitcnt lgkmcnt(0)
	v_mfma_f32_16x16x32_f16 v[26:29], v[198:201], v[176:179], v[26:29]
	v_mfma_f32_16x16x32_f16 v[38:41], v[198:201], v[184:187], v[38:41]
	v_mfma_f32_16x16x32_f16 v[50:53], v[206:209], v[176:179], v[50:53]
	v_mfma_f32_16x16x32_f16 v[62:65], v[206:209], v[184:187], v[62:65]
	v_mfma_f32_16x16x32_f16 v[74:77], v[214:217], v[176:179], v[74:77]
	v_mfma_f32_16x16x32_f16 v[82:85], v[214:217], v[184:187], v[82:85]
	v_mfma_f32_16x16x32_f16 v[90:93], v[222:225], v[176:179], v[90:93]
	v_mfma_f32_16x16x32_f16 v[94:97], v[222:225], v[184:187], v[94:97]
	v_mfma_f32_16x16x32_f16 v[26:29], v[202:205], v[180:183], v[26:29]
	v_mfma_f32_16x16x32_f16 v[38:41], v[202:205], v[188:191], v[38:41]
	v_mfma_f32_16x16x32_f16 v[50:53], v[210:213], v[180:183], v[50:53]
	v_mfma_f32_16x16x32_f16 v[62:65], v[210:213], v[188:191], v[62:65]
	v_mfma_f32_16x16x32_f16 v[74:77], v[218:221], v[180:183], v[74:77]
	v_mfma_f32_16x16x32_f16 v[82:85], v[218:221], v[188:191], v[82:85]
	v_mfma_f32_16x16x32_f16 v[90:93], v[226:229], v[180:183], v[90:93]
	v_mfma_f32_16x16x32_f16 v[94:97], v[226:229], v[188:191], v[94:97]
	s_barrier
	s_mov_b32 m0, s71
	v_lshl_add_u64 v[176:177], v[248:249], 0, s[28:29]
	global_load_lds_dwordx4 v[176:177], off
	s_mov_b32 m0, s72
	v_lshl_add_u64 v[176:177], v[250:251], 0, s[28:29]
	global_load_lds_dwordx4 v[176:177], off
	s_waitcnt vmcnt(6)
	s_barrier
	v_mfma_f32_16x16x32_f16 v[98:101], v[198:201], v[230:233], v[98:101]
	v_mfma_f32_16x16x32_f16 v[102:105], v[198:201], v[238:241], v[102:105]
	v_mfma_f32_16x16x32_f16 v[106:109], v[206:209], v[230:233], v[106:109]
	v_mfma_f32_16x16x32_f16 v[110:113], v[206:209], v[238:241], v[110:113]
	v_mfma_f32_16x16x32_f16 v[114:117], v[214:217], v[230:233], v[114:117]
	v_mfma_f32_16x16x32_f16 v[118:121], v[214:217], v[238:241], v[118:121]
	v_mfma_f32_16x16x32_f16 v[122:125], v[222:225], v[230:233], v[122:125]
	v_mfma_f32_16x16x32_f16 v[126:129], v[222:225], v[238:241], v[126:129]
	v_mfma_f32_16x16x32_f16 v[98:101], v[202:205], v[234:237], v[98:101]
	v_mfma_f32_16x16x32_f16 v[102:105], v[202:205], v[242:245], v[102:105]
	v_mfma_f32_16x16x32_f16 v[106:109], v[210:213], v[234:237], v[106:109]
	v_mfma_f32_16x16x32_f16 v[110:113], v[210:213], v[242:245], v[110:113]
	v_mfma_f32_16x16x32_f16 v[114:117], v[218:221], v[234:237], v[114:117]
	v_mfma_f32_16x16x32_f16 v[118:121], v[218:221], v[242:245], v[118:121]
	v_mfma_f32_16x16x32_f16 v[122:125], v[226:229], v[234:237], v[122:125]
	v_mfma_f32_16x16x32_f16 v[126:129], v[226:229], v[242:245], v[126:129]
	s_barrier
	ds_read_b128 v[176:179], v144
	ds_read_b128 v[180:183], v145
	ds_read_b128 v[184:187], v150
	ds_read_b128 v[188:191], v151
	v_lshl_add_u64 v[230:231], v[192:193], 0, s[28:29]
	s_mov_b32 m0, s73
	ds_read_b128 v[198:201], v173 offset:32768
	ds_read_b128 v[202:205], v173 offset:33792
	ds_read_b128 v[206:209], v173 offset:34816
	ds_read_b128 v[210:213], v173 offset:35840
	ds_read_b128 v[214:217], v173 offset:36864
	ds_read_b128 v[218:221], v173 offset:37888
	ds_read_b128 v[222:225], v173 offset:38912
	ds_read_b128 v[226:229], v173 offset:39936
	global_load_lds_dwordx4 v[230:231], off
	s_mov_b32 m0, s74
	v_lshl_add_u64 v[230:231], v[246:247], 0, s[28:29]
	global_load_lds_dwordx4 v[230:231], off
	s_waitcnt lgkmcnt(8)
	s_barrier
	s_waitcnt lgkmcnt(0)
	v_mfma_f32_16x16x32_f16 v[2:5], v[198:201], v[176:179], v[2:5]
	v_mfma_f32_16x16x32_f16 v[6:9], v[198:201], v[184:187], v[6:9]
	v_mfma_f32_16x16x32_f16 v[10:13], v[206:209], v[176:179], v[10:13]
	v_mfma_f32_16x16x32_f16 v[18:21], v[206:209], v[184:187], v[18:21]
	v_mfma_f32_16x16x32_f16 v[30:33], v[214:217], v[176:179], v[30:33]
	v_mfma_f32_16x16x32_f16 v[42:45], v[214:217], v[184:187], v[42:45]
	v_mfma_f32_16x16x32_f16 v[54:57], v[222:225], v[176:179], v[54:57]
	v_mfma_f32_16x16x32_f16 v[66:69], v[222:225], v[184:187], v[66:69]
	v_mfma_f32_16x16x32_f16 v[2:5], v[202:205], v[180:183], v[2:5]
	v_mfma_f32_16x16x32_f16 v[6:9], v[202:205], v[188:191], v[6:9]
	v_mfma_f32_16x16x32_f16 v[10:13], v[210:213], v[180:183], v[10:13]
	v_mfma_f32_16x16x32_f16 v[18:21], v[210:213], v[188:191], v[18:21]
	v_mfma_f32_16x16x32_f16 v[30:33], v[218:221], v[180:183], v[30:33]
	v_mfma_f32_16x16x32_f16 v[42:45], v[218:221], v[188:191], v[42:45]
	v_mfma_f32_16x16x32_f16 v[54:57], v[226:229], v[180:183], v[54:57]
	v_mfma_f32_16x16x32_f16 v[66:69], v[226:229], v[188:191], v[66:69]
	s_barrier
	v_lshl_add_u64 v[252:253], v[248:249], 0, s[30:31]
	s_mov_b32 m0, s75
	ds_read_b128 v[230:233], v146
	ds_read_b128 v[234:237], v147
	ds_read_b128 v[238:241], v148
	ds_read_b128 v[242:245], v149
	global_load_lds_dwordx4 v[252:253], off
	s_mov_b32 m0, s76
	v_lshl_add_u64 v[252:253], v[250:251], 0, s[30:31]
	global_load_lds_dwordx4 v[252:253], off
	s_barrier
	s_waitcnt lgkmcnt(0)
	v_mfma_f32_16x16x32_f16 v[14:17], v[198:201], v[230:233], v[14:17]
	v_mfma_f32_16x16x32_f16 v[22:25], v[198:201], v[238:241], v[22:25]
	v_mfma_f32_16x16x32_f16 v[34:37], v[206:209], v[230:233], v[34:37]
	v_mfma_f32_16x16x32_f16 v[46:49], v[206:209], v[238:241], v[46:49]
	v_mfma_f32_16x16x32_f16 v[58:61], v[214:217], v[230:233], v[58:61]
	v_mfma_f32_16x16x32_f16 v[70:73], v[214:217], v[238:241], v[70:73]
	v_mfma_f32_16x16x32_f16 v[78:81], v[222:225], v[230:233], v[78:81]
	v_mfma_f32_16x16x32_f16 v[86:89], v[222:225], v[238:241], v[86:89]
	v_mfma_f32_16x16x32_f16 v[14:17], v[202:205], v[234:237], v[14:17]
	v_mfma_f32_16x16x32_f16 v[22:25], v[202:205], v[242:245], v[22:25]
	v_mfma_f32_16x16x32_f16 v[34:37], v[210:213], v[234:237], v[34:37]
	v_mfma_f32_16x16x32_f16 v[46:49], v[210:213], v[242:245], v[46:49]
	v_mfma_f32_16x16x32_f16 v[58:61], v[218:221], v[234:237], v[58:61]
	v_mfma_f32_16x16x32_f16 v[70:73], v[218:221], v[242:245], v[70:73]
	v_mfma_f32_16x16x32_f16 v[78:81], v[226:229], v[234:237], v[78:81]
	v_mfma_f32_16x16x32_f16 v[86:89], v[226:229], v[242:245], v[86:89]
	v_lshl_add_u64 v[192:193], v[192:193], 0, s[30:31]
	s_mov_b32 m0, s77
	s_barrier
	ds_read_b128 v[198:201], v173 offset:49152
	ds_read_b128 v[202:205], v173 offset:50176
	ds_read_b128 v[206:209], v173 offset:51200
	ds_read_b128 v[210:213], v173 offset:52224
	ds_read_b128 v[214:217], v173 offset:53248
	ds_read_b128 v[218:221], v173 offset:54272
	ds_read_b128 v[222:225], v173 offset:55296
	ds_read_b128 v[226:229], v173 offset:56320
	global_load_lds_dwordx4 v[192:193], off
	s_mov_b32 m0, s78
	v_lshl_add_u64 v[192:193], v[246:247], 0, s[30:31]
	global_load_lds_dwordx4 v[192:193], off
	s_barrier
	s_waitcnt lgkmcnt(0)
	v_mfma_f32_16x16x32_f16 v[26:29], v[198:201], v[176:179], v[26:29]
	v_mfma_f32_16x16x32_f16 v[38:41], v[198:201], v[184:187], v[38:41]
	v_mfma_f32_16x16x32_f16 v[50:53], v[206:209], v[176:179], v[50:53]
	v_mfma_f32_16x16x32_f16 v[62:65], v[206:209], v[184:187], v[62:65]
	v_mfma_f32_16x16x32_f16 v[74:77], v[214:217], v[176:179], v[74:77]
	v_mfma_f32_16x16x32_f16 v[82:85], v[214:217], v[184:187], v[82:85]
	v_mfma_f32_16x16x32_f16 v[90:93], v[222:225], v[176:179], v[90:93]
	v_mfma_f32_16x16x32_f16 v[94:97], v[222:225], v[184:187], v[94:97]
	v_mfma_f32_16x16x32_f16 v[26:29], v[202:205], v[180:183], v[26:29]
	v_mfma_f32_16x16x32_f16 v[38:41], v[202:205], v[188:191], v[38:41]
	v_mfma_f32_16x16x32_f16 v[50:53], v[210:213], v[180:183], v[50:53]
	v_mfma_f32_16x16x32_f16 v[62:65], v[210:213], v[188:191], v[62:65]
	v_mfma_f32_16x16x32_f16 v[74:77], v[218:221], v[180:183], v[74:77]
	v_mfma_f32_16x16x32_f16 v[82:85], v[218:221], v[188:191], v[82:85]
	v_mfma_f32_16x16x32_f16 v[90:93], v[226:229], v[180:183], v[90:93]
	v_mfma_f32_16x16x32_f16 v[94:97], v[226:229], v[188:191], v[94:97]
	s_barrier
	s_mov_b32 m0, s79
	v_lshl_add_u64 v[176:177], v[248:249], 0, s[34:35]
	global_load_lds_dwordx4 v[176:177], off
	s_mov_b32 m0, s80
	v_lshl_add_u64 v[176:177], v[250:251], 0, s[34:35]
	global_load_lds_dwordx4 v[176:177], off
	s_waitcnt vmcnt(6)
	s_barrier
	v_mfma_f32_16x16x32_f16 v[98:101], v[198:201], v[230:233], v[98:101]
	v_mfma_f32_16x16x32_f16 v[102:105], v[198:201], v[238:241], v[102:105]
	v_mfma_f32_16x16x32_f16 v[106:109], v[206:209], v[230:233], v[106:109]
	v_mfma_f32_16x16x32_f16 v[110:113], v[206:209], v[238:241], v[110:113]
	v_mfma_f32_16x16x32_f16 v[114:117], v[214:217], v[230:233], v[114:117]
	v_mfma_f32_16x16x32_f16 v[118:121], v[214:217], v[238:241], v[118:121]
	v_mfma_f32_16x16x32_f16 v[122:125], v[222:225], v[230:233], v[122:125]
	v_mfma_f32_16x16x32_f16 v[126:129], v[222:225], v[238:241], v[126:129]
	v_mfma_f32_16x16x32_f16 v[98:101], v[202:205], v[234:237], v[98:101]
	v_mfma_f32_16x16x32_f16 v[102:105], v[202:205], v[242:245], v[102:105]
	v_mfma_f32_16x16x32_f16 v[106:109], v[210:213], v[234:237], v[106:109]
	v_mfma_f32_16x16x32_f16 v[110:113], v[210:213], v[242:245], v[110:113]
	v_mfma_f32_16x16x32_f16 v[114:117], v[218:221], v[234:237], v[114:117]
	v_mfma_f32_16x16x32_f16 v[118:121], v[218:221], v[242:245], v[118:121]
	v_mfma_f32_16x16x32_f16 v[122:125], v[226:229], v[234:237], v[122:125]
	v_mfma_f32_16x16x32_f16 v[126:129], v[226:229], v[242:245], v[126:129]
	s_add_i32 s44, s44, 2
	s_add_u32 s42, s42, 0x100
	s_addc_u32 s43, s43, 0
	s_cmp_lt_u32 s44, 4
	s_barrier
	s_cbranch_scc1 .LBB9_38
	s_add_u32 s40, s40, 0x20380
	s_addc_u32 s41, s41, 0
	v_readfirstlane_b32 s39, v174
	v_lshl_add_u64 v[130:131], v[130:131], 1, s[40:41]
	s_mov_b32 m0, s39
	v_readfirstlane_b32 s39, v175
	ds_read_b128 v[134:137], v169
	ds_read_b128 v[138:141], v170
	ds_read_b128 v[152:155], v171
	ds_read_b128 v[156:159], v172
	ds_read_b128 v[166:169], v173
	ds_read_b128 v[176:179], v173 offset:1024
	ds_read_b128 v[180:183], v173 offset:2048
	ds_read_b128 v[184:187], v173 offset:3072
	ds_read_b128 v[188:191], v173 offset:4096
	ds_read_b128 v[198:201], v173 offset:5120
	ds_read_b128 v[202:205], v173 offset:6144
	ds_read_b128 v[206:209], v173 offset:7168
	global_load_lds_dwordx4 v[130:131], off
	s_mov_b32 m0, s39
	v_lshl_add_u64 v[130:131], v[132:133], 1, s[40:41]
	global_load_lds_dwordx4 v[130:131], off
	s_barrier
	s_waitcnt lgkmcnt(0)
	v_mfma_f32_16x16x32_f16 v[2:5], v[166:169], v[134:137], v[2:5]
	v_mfma_f32_16x16x32_f16 v[6:9], v[166:169], v[152:155], v[6:9]
	v_mfma_f32_16x16x32_f16 v[30:33], v[188:191], v[134:137], v[30:33]
	v_mfma_f32_16x16x32_f16 v[2:5], v[176:179], v[138:141], v[2:5]
	v_mfma_f32_16x16x32_f16 v[6:9], v[176:179], v[156:159], v[6:9]
	v_mfma_f32_16x16x32_f16 v[10:13], v[180:183], v[134:137], v[10:13]
	v_mfma_f32_16x16x32_f16 v[18:21], v[180:183], v[152:155], v[18:21]
	v_mfma_f32_16x16x32_f16 v[30:33], v[198:201], v[138:141], v[30:33]
	v_mfma_f32_16x16x32_f16 v[42:45], v[188:191], v[152:155], v[42:45]
	v_mfma_f32_16x16x32_f16 v[54:57], v[202:205], v[134:137], v[54:57]
	v_mfma_f32_16x16x32_f16 v[66:69], v[202:205], v[152:155], v[66:69]
	v_mfma_f32_16x16x32_f16 v[10:13], v[184:187], v[138:141], v[10:13]
	v_mfma_f32_16x16x32_f16 v[18:21], v[184:187], v[156:159], v[18:21]
	v_mfma_f32_16x16x32_f16 v[42:45], v[198:201], v[156:159], v[42:45]
	v_mfma_f32_16x16x32_f16 v[54:57], v[206:209], v[138:141], v[54:57]
	v_mfma_f32_16x16x32_f16 v[66:69], v[206:209], v[156:159], v[66:69]
	s_barrier
	ds_read_b128 v[130:133], v161
	ds_read_b128 v[210:213], v162
	ds_read_b128 v[160:163], v163
	ds_read_b128 v[214:217], v164
	s_barrier
	s_waitcnt lgkmcnt(0)
	v_mfma_f32_16x16x32_f16 v[58:61], v[188:191], v[130:133], v[58:61]
	v_mfma_f32_16x16x32_f16 v[14:17], v[166:169], v[130:133], v[14:17]
	v_mfma_f32_16x16x32_f16 v[22:25], v[166:169], v[160:163], v[22:25]
	v_mfma_f32_16x16x32_f16 v[164:167], v[198:201], v[210:213], v[58:61]
	v_mfma_f32_16x16x32_f16 v[58:61], v[188:191], v[160:163], v[70:73]
	v_mfma_f32_16x16x32_f16 v[46:49], v[180:183], v[160:163], v[46:49]
	v_mfma_f32_16x16x32_f16 v[168:171], v[198:201], v[214:217], v[58:61]
	v_mfma_f32_16x16x32_f16 v[58:61], v[202:205], v[130:133], v[78:81]
	v_mfma_f32_16x16x32_f16 v[14:17], v[176:179], v[210:213], v[14:17]
	v_mfma_f32_16x16x32_f16 v[34:37], v[180:183], v[130:133], v[34:37]
	v_mfma_f32_16x16x32_f16 v[46:49], v[184:187], v[214:217], v[46:49]
	v_mfma_f32_16x16x32_f16 v[78:81], v[206:209], v[210:213], v[58:61]
	v_mfma_f32_16x16x32_f16 v[58:61], v[202:205], v[160:163], v[86:89]
	v_mfma_f32_16x16x32_f16 v[22:25], v[176:179], v[214:217], v[22:25]
	v_mfma_f32_16x16x32_f16 v[34:37], v[184:187], v[210:213], v[34:37]
	v_mfma_f32_16x16x32_f16 v[86:89], v[206:209], v[214:217], v[58:61]
	s_barrier
	s_nop 2
	ds_read_b128 v[58:61], v173 offset:16384
	ds_read_b128 v[70:73], v173 offset:17408
	ds_read_b128 v[174:177], v173 offset:18432
	ds_read_b128 v[178:181], v173 offset:19456
	ds_read_b128 v[182:185], v173 offset:20480
	ds_read_b128 v[186:189], v173 offset:21504
	ds_read_b128 v[190:193], v173 offset:22528
	ds_read_b128 v[198:201], v173 offset:23552
	s_waitcnt vmcnt(4)
	s_barrier
	s_waitcnt lgkmcnt(0)
	v_mfma_f32_16x16x32_f16 v[26:29], v[58:61], v[134:137], v[26:29]
	v_mfma_f32_16x16x32_f16 v[26:29], v[70:73], v[138:141], v[26:29]
	v_mfma_f32_16x16x32_f16 v[38:41], v[58:61], v[152:155], v[38:41]
	v_mfma_f32_16x16x32_f16 v[50:53], v[174:177], v[134:137], v[50:53]
	v_mfma_f32_16x16x32_f16 v[62:65], v[174:177], v[152:155], v[62:65]
	v_mfma_f32_16x16x32_f16 v[74:77], v[182:185], v[134:137], v[74:77]
	v_mfma_f32_16x16x32_f16 v[82:85], v[182:185], v[152:155], v[82:85]
	v_mfma_f32_16x16x32_f16 v[90:93], v[190:193], v[134:137], v[90:93]
	v_mfma_f32_16x16x32_f16 v[94:97], v[190:193], v[152:155], v[94:97]
	v_mfma_f32_16x16x32_f16 v[38:41], v[70:73], v[156:159], v[38:41]
	v_mfma_f32_16x16x32_f16 v[50:53], v[178:181], v[138:141], v[50:53]
	v_mfma_f32_16x16x32_f16 v[62:65], v[178:181], v[156:159], v[62:65]
	v_mfma_f32_16x16x32_f16 v[74:77], v[186:189], v[138:141], v[74:77]
	v_mfma_f32_16x16x32_f16 v[82:85], v[186:189], v[156:159], v[82:85]
	v_mfma_f32_16x16x32_f16 v[90:93], v[198:201], v[138:141], v[90:93]
	v_mfma_f32_16x16x32_f16 v[94:97], v[198:201], v[156:159], v[94:97]
	v_mfma_f32_16x16x32_f16 v[98:101], v[58:61], v[130:133], v[98:101]
	v_mfma_f32_16x16x32_f16 v[58:61], v[58:61], v[160:163], v[102:105]
	v_mfma_f32_16x16x32_f16 v[102:105], v[70:73], v[214:217], v[58:61]
	v_mfma_f32_16x16x32_f16 v[58:61], v[174:177], v[130:133], v[106:109]
	v_mfma_f32_16x16x32_f16 v[106:109], v[178:181], v[210:213], v[58:61]
	v_mfma_f32_16x16x32_f16 v[58:61], v[174:177], v[160:163], v[110:113]
	v_mfma_f32_16x16x32_f16 v[202:205], v[178:181], v[214:217], v[58:61]
	v_mfma_f32_16x16x32_f16 v[58:61], v[182:185], v[130:133], v[114:117]
	v_mfma_f32_16x16x32_f16 v[206:209], v[186:189], v[210:213], v[58:61]
	v_mfma_f32_16x16x32_f16 v[58:61], v[182:185], v[160:163], v[118:121]
	v_mfma_f32_16x16x32_f16 v[218:221], v[186:189], v[214:217], v[58:61]
	v_mfma_f32_16x16x32_f16 v[58:61], v[190:193], v[130:133], v[122:125]
	v_mfma_f32_16x16x32_f16 v[98:101], v[70:73], v[210:213], v[98:101]
	v_mfma_f32_16x16x32_f16 v[210:213], v[198:201], v[210:213], v[58:61]
	v_mfma_f32_16x16x32_f16 v[58:61], v[190:193], v[160:163], v[126:129]
	v_mfma_f32_16x16x32_f16 v[198:201], v[198:201], v[214:217], v[58:61]
	s_barrier
	ds_read_b128 v[110:113], v144
	ds_read_b128 v[130:133], v145
	ds_read_b128 v[214:217], v150
	ds_read_b128 v[222:225], v151
	s_nop 0
	ds_read_b128 v[58:61], v173 offset:32768
	ds_read_b128 v[70:73], v173 offset:33792
	ds_read_b128 v[114:117], v173 offset:34816
	ds_read_b128 v[118:121], v173 offset:35840
	ds_read_b128 v[134:137], v173 offset:36864
	ds_read_b128 v[138:141], v173 offset:37888
	ds_read_b128 v[178:181], v173 offset:38912
	ds_read_b128 v[226:229], v173 offset:39936
	s_waitcnt vmcnt(2)
	s_barrier
	s_waitcnt lgkmcnt(0)
	v_mfma_f32_16x16x32_f16 v[2:5], v[58:61], v[110:113], v[2:5]
	v_mfma_f32_16x16x32_f16 v[190:193], v[70:73], v[130:133], v[2:5]
	v_mfma_f32_16x16x32_f16 v[2:5], v[58:61], v[214:217], v[6:9]
	v_mfma_f32_16x16x32_f16 v[158:161], v[70:73], v[222:225], v[2:5]
	v_mfma_f32_16x16x32_f16 v[2:5], v[114:117], v[110:113], v[10:13]
	v_mfma_f32_16x16x32_f16 v[186:189], v[118:121], v[130:133], v[2:5]
	v_mfma_f32_16x16x32_f16 v[2:5], v[114:117], v[214:217], v[18:21]
	v_mfma_f32_16x16x32_f16 v[154:157], v[118:121], v[222:225], v[2:5]
	v_mfma_f32_16x16x32_f16 v[2:5], v[134:137], v[110:113], v[30:33]
	v_mfma_f32_16x16x32_f16 v[182:185], v[138:141], v[130:133], v[2:5]
	v_mfma_f32_16x16x32_f16 v[2:5], v[134:137], v[214:217], v[42:45]
	v_mfma_f32_16x16x32_f16 v[150:153], v[138:141], v[222:225], v[2:5]
	v_mfma_f32_16x16x32_f16 v[2:5], v[178:181], v[110:113], v[54:57]
	v_mfma_f32_16x16x32_f16 v[174:177], v[226:229], v[130:133], v[2:5]
	v_mfma_f32_16x16x32_f16 v[2:5], v[178:181], v[214:217], v[66:69]
	v_mfma_f32_16x16x32_f16 v[142:145], v[226:229], v[222:225], v[2:5]
	s_barrier
	s_nop 4
	ds_read_b128 v[2:5], v146
	ds_read_b128 v[10:13], v147
	ds_read_b128 v[18:21], v148
	ds_read_b128 v[42:45], v149
	s_waitcnt vmcnt(0)
	s_barrier
	s_waitcnt lgkmcnt(0)
	v_mfma_f32_16x16x32_f16 v[6:9], v[58:61], v[2:5], v[14:17]
	v_mfma_f32_16x16x32_f16 v[126:129], v[70:73], v[10:13], v[6:9]
	v_mfma_f32_16x16x32_f16 v[6:9], v[58:61], v[18:21], v[22:25]
	v_mfma_f32_16x16x32_f16 v[70:73], v[70:73], v[42:45], v[6:9]
	v_mfma_f32_16x16x32_f16 v[6:9], v[114:117], v[2:5], v[34:37]
	v_mfma_f32_16x16x32_f16 v[122:125], v[118:121], v[10:13], v[6:9]
	v_mfma_f32_16x16x32_f16 v[6:9], v[114:117], v[18:21], v[46:49]
	v_mfma_f32_16x16x32_f16 v[58:61], v[118:121], v[42:45], v[6:9]
	v_mfma_f32_16x16x32_f16 v[6:9], v[134:137], v[2:5], v[164:167]
	v_mfma_f32_16x16x32_f16 v[118:121], v[138:141], v[10:13], v[6:9]
	v_mfma_f32_16x16x32_f16 v[6:9], v[134:137], v[18:21], v[168:171]
	v_mfma_f32_16x16x32_f16 v[46:49], v[138:141], v[42:45], v[6:9]
	v_mfma_f32_16x16x32_f16 v[6:9], v[178:181], v[2:5], v[78:81]
	v_mfma_f32_16x16x32_f16 v[114:117], v[226:229], v[10:13], v[6:9]
	v_mfma_f32_16x16x32_f16 v[6:9], v[178:181], v[18:21], v[86:89]
	v_mfma_f32_16x16x32_f16 v[30:33], v[226:229], v[42:45], v[6:9]
	s_barrier
	s_nop 4
	ds_read_b128 v[6:9], v173 offset:49152
	ds_read_b128 v[14:17], v173 offset:50176
	ds_read_b128 v[22:25], v173 offset:51200
	ds_read_b128 v[34:37], v173 offset:52224
	ds_read_b128 v[54:57], v173 offset:53248
	ds_read_b128 v[66:69], v173 offset:54272
	ds_read_b128 v[78:81], v173 offset:55296
	ds_read_b128 v[86:89], v173 offset:56320
	s_barrier
	s_waitcnt lgkmcnt(0)
	v_mfma_f32_16x16x32_f16 v[26:29], v[6:9], v[110:113], v[26:29]
	v_mfma_f32_16x16x32_f16 v[178:181], v[14:17], v[130:133], v[26:29]
	v_mfma_f32_16x16x32_f16 v[26:29], v[6:9], v[214:217], v[38:41]
	v_mfma_f32_16x16x32_f16 v[146:149], v[14:17], v[222:225], v[26:29]
	v_mfma_f32_16x16x32_f16 v[26:29], v[22:25], v[110:113], v[50:53]
	v_mfma_f32_16x16x32_f16 v[170:173], v[34:37], v[130:133], v[26:29]
	v_mfma_f32_16x16x32_f16 v[26:29], v[22:25], v[214:217], v[62:65]
	v_mfma_f32_16x16x32_f16 v[138:141], v[34:37], v[222:225], v[26:29]
	v_mfma_f32_16x16x32_f16 v[26:29], v[54:57], v[110:113], v[74:77]
	v_mfma_f32_16x16x32_f16 v[166:169], v[66:69], v[130:133], v[26:29]
	v_mfma_f32_16x16x32_f16 v[26:29], v[54:57], v[214:217], v[82:85]
	v_mfma_f32_16x16x32_f16 v[134:137], v[66:69], v[222:225], v[26:29]
	v_mfma_f32_16x16x32_f16 v[26:29], v[78:81], v[110:113], v[90:93]
	v_mfma_f32_16x16x32_f16 v[162:165], v[86:89], v[130:133], v[26:29]
	v_mfma_f32_16x16x32_f16 v[26:29], v[78:81], v[214:217], v[94:97]
	v_mfma_f32_16x16x32_f16 v[130:133], v[86:89], v[222:225], v[26:29]
	v_mfma_f32_16x16x32_f16 v[26:29], v[6:9], v[2:5], v[98:101]
	v_mfma_f32_16x16x32_f16 v[6:9], v[6:9], v[18:21], v[102:105]
	v_mfma_f32_16x16x32_f16 v[110:113], v[14:17], v[10:13], v[26:29]
	v_mfma_f32_16x16x32_f16 v[26:29], v[14:17], v[42:45], v[6:9]
	v_mfma_f32_16x16x32_f16 v[6:9], v[22:25], v[2:5], v[106:109]
	v_mfma_f32_16x16x32_f16 v[106:109], v[34:37], v[10:13], v[6:9]
	v_mfma_f32_16x16x32_f16 v[6:9], v[22:25], v[18:21], v[202:205]
	v_mfma_f32_16x16x32_f16 v[14:17], v[34:37], v[42:45], v[6:9]
	v_mfma_f32_16x16x32_f16 v[6:9], v[54:57], v[2:5], v[206:209]
	v_mfma_f32_16x16x32_f16 v[2:5], v[78:81], v[2:5], v[210:213]
	v_mfma_f32_16x16x32_f16 v[102:105], v[66:69], v[10:13], v[6:9]
	v_mfma_f32_16x16x32_f16 v[6:9], v[54:57], v[18:21], v[218:221]
	v_mfma_f32_16x16x32_f16 v[98:101], v[86:89], v[10:13], v[2:5]
	v_mfma_f32_16x16x32_f16 v[2:5], v[78:81], v[18:21], v[198:201]
	v_mfma_f32_16x16x32_f16 v[6:9], v[66:69], v[42:45], v[6:9]
	v_mfma_f32_16x16x32_f16 v[2:5], v[86:89], v[42:45], v[2:5]
	s_cmpk_gt_u32 s54, 0xff
	s_barrier
	s_cbranch_scc1 .LBB9_34
	s_barrier
	s_branch .LBB9_34

.LBB10_12:
	ds_read_b128 v[182:185], v171
	ds_read_b128 v[186:189], v173
	ds_read_b128 v[190:193], v174
	ds_read_b128 v[194:197], v175
	v_add_u32_e32 v177, 0xc000, v148
	v_lshl_add_u64 v[246:247], v[136:137], 0, s[44:45]
	v_add_u32_e32 v176, s63, v170
	v_lshl_add_u64 v[178:179], v[246:247], 0, s[28:29]
	s_mov_b32 m0, s70
	ds_read_b128 v[198:201], v176
	ds_read_b128 v[202:205], v176 offset:1024
	ds_read_b128 v[206:209], v176 offset:2048
	ds_read_b128 v[210:213], v176 offset:3072
	ds_read_b128 v[214:217], v176 offset:4096
	ds_read_b128 v[218:221], v176 offset:5120
	ds_read_b128 v[222:225], v176 offset:6144
	ds_read_b128 v[226:229], v176 offset:7168
	global_load_lds_dwordx4 v[178:179], off
	v_add_u32_e32 v178, 0xe000, v148
	v_lshl_add_u64 v[248:249], v[134:135], 0, s[44:45]
	s_mov_b32 m0, s71
	v_lshl_add_u64 v[230:231], v[248:249], 0, s[28:29]
	global_load_lds_dwordx4 v[230:231], off
	s_waitcnt lgkmcnt(8)
	s_barrier
	s_waitcnt lgkmcnt(0)
	v_mfma_f32_16x16x32_f16 v[126:129], v[198:201], v[182:185], v[126:129]
	v_mfma_f32_16x16x32_f16 v[122:125], v[198:201], v[190:193], v[122:125]
	v_mfma_f32_16x16x32_f16 v[118:121], v[206:209], v[182:185], v[118:121]
	v_mfma_f32_16x16x32_f16 v[114:117], v[206:209], v[190:193], v[114:117]
	v_mfma_f32_16x16x32_f16 v[110:113], v[214:217], v[182:185], v[110:113]
	v_mfma_f32_16x16x32_f16 v[106:109], v[214:217], v[190:193], v[106:109]
	v_mfma_f32_16x16x32_f16 v[102:105], v[222:225], v[182:185], v[102:105]
	v_mfma_f32_16x16x32_f16 v[98:101], v[222:225], v[190:193], v[98:101]
	v_mfma_f32_16x16x32_f16 v[126:129], v[202:205], v[186:189], v[126:129]
	v_mfma_f32_16x16x32_f16 v[122:125], v[202:205], v[194:197], v[122:125]
	v_mfma_f32_16x16x32_f16 v[118:121], v[210:213], v[186:189], v[118:121]
	v_mfma_f32_16x16x32_f16 v[114:117], v[210:213], v[194:197], v[114:117]
	v_mfma_f32_16x16x32_f16 v[110:113], v[218:221], v[186:189], v[110:113]
	v_mfma_f32_16x16x32_f16 v[106:109], v[218:221], v[194:197], v[106:109]
	v_mfma_f32_16x16x32_f16 v[102:105], v[226:229], v[186:189], v[102:105]
	v_mfma_f32_16x16x32_f16 v[98:101], v[226:229], v[194:197], v[98:101]
	s_barrier
	v_lshl_add_u64 v[250:251], v[140:141], 0, s[44:45]
	v_lshl_add_u64 v[252:253], v[250:251], 0, s[30:31]
	s_mov_b32 m0, s72
	ds_read_b128 v[230:233], v162
	ds_read_b128 v[234:237], v163
	ds_read_b128 v[238:241], v164
	ds_read_b128 v[242:245], v165
	global_load_lds_dwordx4 v[252:253], off
	v_lshl_add_u64 v[252:253], v[138:139], 0, s[44:45]
	s_mov_b32 m0, s73
	v_lshl_add_u64 v[254:255], v[252:253], 0, s[30:31]
	global_load_lds_dwordx4 v[254:255], off
	s_barrier
	s_waitcnt lgkmcnt(0)
	v_mfma_f32_16x16x32_f16 v[94:97], v[198:201], v[230:233], v[94:97]
	v_mfma_f32_16x16x32_f16 v[90:93], v[198:201], v[238:241], v[90:93]
	v_mfma_f32_16x16x32_f16 v[86:89], v[206:209], v[230:233], v[86:89]
	v_mfma_f32_16x16x32_f16 v[82:85], v[206:209], v[238:241], v[82:85]
	v_mfma_f32_16x16x32_f16 v[78:81], v[214:217], v[230:233], v[78:81]
	v_mfma_f32_16x16x32_f16 v[74:77], v[214:217], v[238:241], v[74:77]
	v_mfma_f32_16x16x32_f16 v[70:73], v[222:225], v[230:233], v[70:73]
	v_mfma_f32_16x16x32_f16 v[66:69], v[222:225], v[238:241], v[66:69]
	v_mfma_f32_16x16x32_f16 v[94:97], v[202:205], v[234:237], v[94:97]
	v_mfma_f32_16x16x32_f16 v[90:93], v[202:205], v[242:245], v[90:93]
	v_mfma_f32_16x16x32_f16 v[86:89], v[210:213], v[234:237], v[86:89]
	v_mfma_f32_16x16x32_f16 v[82:85], v[210:213], v[242:245], v[82:85]
	v_mfma_f32_16x16x32_f16 v[78:81], v[218:221], v[234:237], v[78:81]
	v_mfma_f32_16x16x32_f16 v[74:77], v[218:221], v[242:245], v[74:77]
	v_mfma_f32_16x16x32_f16 v[70:73], v[226:229], v[234:237], v[70:73]
	v_mfma_f32_16x16x32_f16 v[66:69], v[226:229], v[242:245], v[66:69]
	v_lshl_add_u64 v[254:255], v[246:247], 0, s[30:31]
	s_mov_b32 m0, s74
	s_barrier
	ds_read_b128 v[198:201], v176 offset:16384
	ds_read_b128 v[202:205], v176 offset:17408
	ds_read_b128 v[206:209], v176 offset:18432
	ds_read_b128 v[210:213], v176 offset:19456
	ds_read_b128 v[214:217], v176 offset:20480
	ds_read_b128 v[218:221], v176 offset:21504
	ds_read_b128 v[222:225], v176 offset:22528
	ds_read_b128 v[226:229], v176 offset:23552
	global_load_lds_dwordx4 v[254:255], off
	s_mov_b32 m0, s75
	v_lshl_add_u64 v[254:255], v[248:249], 0, s[30:31]
	global_load_lds_dwordx4 v[254:255], off
	s_barrier
	s_waitcnt lgkmcnt(0)
	v_mfma_f32_16x16x32_f16 v[62:65], v[198:201], v[182:185], v[62:65]
	v_mfma_f32_16x16x32_f16 v[58:61], v[198:201], v[190:193], v[58:61]
	v_mfma_f32_16x16x32_f16 v[54:57], v[206:209], v[182:185], v[54:57]
	v_mfma_f32_16x16x32_f16 v[50:53], v[206:209], v[190:193], v[50:53]
	v_mfma_f32_16x16x32_f16 v[46:49], v[214:217], v[182:185], v[46:49]
	v_mfma_f32_16x16x32_f16 v[42:45], v[214:217], v[190:193], v[42:45]
	v_mfma_f32_16x16x32_f16 v[38:41], v[222:225], v[182:185], v[38:41]
	v_mfma_f32_16x16x32_f16 v[34:37], v[222:225], v[190:193], v[34:37]
	v_mfma_f32_16x16x32_f16 v[62:65], v[202:205], v[186:189], v[62:65]
	v_mfma_f32_16x16x32_f16 v[58:61], v[202:205], v[194:197], v[58:61]
	v_mfma_f32_16x16x32_f16 v[54:57], v[210:213], v[186:189], v[54:57]
	v_mfma_f32_16x16x32_f16 v[50:53], v[210:213], v[194:197], v[50:53]
	v_mfma_f32_16x16x32_f16 v[46:49], v[218:221], v[186:189], v[46:49]
	v_mfma_f32_16x16x32_f16 v[42:45], v[218:221], v[194:197], v[42:45]
	v_mfma_f32_16x16x32_f16 v[38:41], v[226:229], v[186:189], v[38:41]
	v_mfma_f32_16x16x32_f16 v[34:37], v[226:229], v[194:197], v[34:37]
	s_barrier
	s_mov_b32 m0, s76
	v_lshl_add_u64 v[182:183], v[250:251], 0, s[34:35]
	global_load_lds_dwordx4 v[182:183], off
	s_mov_b32 m0, s77
	v_lshl_add_u64 v[182:183], v[252:253], 0, s[34:35]
	global_load_lds_dwordx4 v[182:183], off
	s_waitcnt vmcnt(6)
	s_barrier
	v_mfma_f32_16x16x32_f16 v[30:33], v[198:201], v[230:233], v[30:33]
	v_mfma_f32_16x16x32_f16 v[26:29], v[198:201], v[238:241], v[26:29]
	v_mfma_f32_16x16x32_f16 v[22:25], v[206:209], v[230:233], v[22:25]
	v_mfma_f32_16x16x32_f16 v[18:21], v[206:209], v[238:241], v[18:21]
	v_mfma_f32_16x16x32_f16 v[14:17], v[214:217], v[230:233], v[14:17]
	v_mfma_f32_16x16x32_f16 v[10:13], v[214:217], v[238:241], v[10:13]
	v_mfma_f32_16x16x32_f16 v[6:9], v[222:225], v[230:233], v[6:9]
	v_mfma_f32_16x16x32_f16 v[2:5], v[222:225], v[238:241], v[2:5]
	v_mfma_f32_16x16x32_f16 v[30:33], v[202:205], v[234:237], v[30:33]
	v_mfma_f32_16x16x32_f16 v[26:29], v[202:205], v[242:245], v[26:29]
	v_mfma_f32_16x16x32_f16 v[22:25], v[210:213], v[234:237], v[22:25]
	v_mfma_f32_16x16x32_f16 v[18:21], v[210:213], v[242:245], v[18:21]
	v_mfma_f32_16x16x32_f16 v[14:17], v[218:221], v[234:237], v[14:17]
	v_mfma_f32_16x16x32_f16 v[10:13], v[218:221], v[242:245], v[10:13]
	v_mfma_f32_16x16x32_f16 v[6:9], v[226:229], v[234:237], v[6:9]
	v_mfma_f32_16x16x32_f16 v[2:5], v[226:229], v[242:245], v[2:5]
	s_barrier
	ds_read_b128 v[182:185], v144
	ds_read_b128 v[186:189], v145
	ds_read_b128 v[190:193], v146
	ds_read_b128 v[194:197], v147
	v_lshl_add_u64 v[230:231], v[246:247], 0, s[34:35]
	s_mov_b32 m0, s78
	ds_read_b128 v[198:201], v176 offset:32768
	ds_read_b128 v[202:205], v176 offset:33792
	ds_read_b128 v[206:209], v176 offset:34816
	ds_read_b128 v[210:213], v176 offset:35840
	ds_read_b128 v[214:217], v176 offset:36864
	ds_read_b128 v[218:221], v176 offset:37888
	ds_read_b128 v[222:225], v176 offset:38912
	ds_read_b128 v[226:229], v176 offset:39936
	global_load_lds_dwordx4 v[230:231], off
	s_mov_b32 m0, s79
	v_lshl_add_u64 v[230:231], v[248:249], 0, s[34:35]
	global_load_lds_dwordx4 v[230:231], off
	s_waitcnt lgkmcnt(8)
	s_barrier
	s_waitcnt lgkmcnt(0)
	v_mfma_f32_16x16x32_f16 v[126:129], v[198:201], v[182:185], v[126:129]
	v_mfma_f32_16x16x32_f16 v[122:125], v[198:201], v[190:193], v[122:125]
	v_mfma_f32_16x16x32_f16 v[118:121], v[206:209], v[182:185], v[118:121]
	v_mfma_f32_16x16x32_f16 v[114:117], v[206:209], v[190:193], v[114:117]
	v_mfma_f32_16x16x32_f16 v[110:113], v[214:217], v[182:185], v[110:113]
	v_mfma_f32_16x16x32_f16 v[106:109], v[214:217], v[190:193], v[106:109]
	v_mfma_f32_16x16x32_f16 v[102:105], v[222:225], v[182:185], v[102:105]
	v_mfma_f32_16x16x32_f16 v[98:101], v[222:225], v[190:193], v[98:101]
	v_mfma_f32_16x16x32_f16 v[126:129], v[202:205], v[186:189], v[126:129]
	v_mfma_f32_16x16x32_f16 v[122:125], v[202:205], v[194:197], v[122:125]
	v_mfma_f32_16x16x32_f16 v[118:121], v[210:213], v[186:189], v[118:121]
	v_mfma_f32_16x16x32_f16 v[114:117], v[210:213], v[194:197], v[114:117]
	v_mfma_f32_16x16x32_f16 v[110:113], v[218:221], v[186:189], v[110:113]
	v_mfma_f32_16x16x32_f16 v[106:109], v[218:221], v[194:197], v[106:109]
	v_mfma_f32_16x16x32_f16 v[102:105], v[226:229], v[186:189], v[102:105]
	v_mfma_f32_16x16x32_f16 v[98:101], v[226:229], v[194:197], v[98:101]
	s_barrier
	v_lshl_add_u64 v[254:255], v[250:251], 0, s[36:37]
	s_mov_b32 m0, s80
	ds_read_b128 v[230:233], v150
	ds_read_b128 v[234:237], v151
	ds_read_b128 v[238:241], v152
	ds_read_b128 v[242:245], v153
	global_load_lds_dwordx4 v[254:255], off
	s_mov_b32 m0, s81
	v_lshl_add_u64 v[254:255], v[252:253], 0, s[36:37]
	global_load_lds_dwordx4 v[254:255], off
	s_barrier
	s_waitcnt lgkmcnt(0)
	v_mfma_f32_16x16x32_f16 v[94:97], v[198:201], v[230:233], v[94:97]
	v_mfma_f32_16x16x32_f16 v[90:93], v[198:201], v[238:241], v[90:93]
	v_mfma_f32_16x16x32_f16 v[86:89], v[206:209], v[230:233], v[86:89]
	v_mfma_f32_16x16x32_f16 v[82:85], v[206:209], v[238:241], v[82:85]
	v_mfma_f32_16x16x32_f16 v[78:81], v[214:217], v[230:233], v[78:81]
	v_mfma_f32_16x16x32_f16 v[74:77], v[214:217], v[238:241], v[74:77]
	v_mfma_f32_16x16x32_f16 v[70:73], v[222:225], v[230:233], v[70:73]
	v_mfma_f32_16x16x32_f16 v[66:69], v[222:225], v[238:241], v[66:69]
	v_mfma_f32_16x16x32_f16 v[94:97], v[202:205], v[234:237], v[94:97]
	v_mfma_f32_16x16x32_f16 v[90:93], v[202:205], v[242:245], v[90:93]
	v_mfma_f32_16x16x32_f16 v[86:89], v[210:213], v[234:237], v[86:89]
	v_mfma_f32_16x16x32_f16 v[82:85], v[210:213], v[242:245], v[82:85]
	v_mfma_f32_16x16x32_f16 v[78:81], v[218:221], v[234:237], v[78:81]
	v_mfma_f32_16x16x32_f16 v[74:77], v[218:221], v[242:245], v[74:77]
	v_mfma_f32_16x16x32_f16 v[70:73], v[226:229], v[234:237], v[70:73]
	v_mfma_f32_16x16x32_f16 v[66:69], v[226:229], v[242:245], v[66:69]
	v_lshl_add_u64 v[246:247], v[246:247], 0, s[36:37]
	s_mov_b32 m0, s82
	s_barrier
	ds_read_b128 v[198:201], v176 offset:49152
	ds_read_b128 v[202:205], v176 offset:50176
	ds_read_b128 v[206:209], v176 offset:51200
	ds_read_b128 v[210:213], v176 offset:52224
	ds_read_b128 v[214:217], v176 offset:53248
	ds_read_b128 v[218:221], v176 offset:54272
	ds_read_b128 v[222:225], v176 offset:55296
	ds_read_b128 v[226:229], v176 offset:56320
	global_load_lds_dwordx4 v[246:247], off
	s_mov_b32 m0, s83
	v_lshl_add_u64 v[246:247], v[248:249], 0, s[36:37]
	global_load_lds_dwordx4 v[246:247], off
	s_barrier
	s_waitcnt lgkmcnt(0)
	v_mfma_f32_16x16x32_f16 v[62:65], v[198:201], v[182:185], v[62:65]
	v_mfma_f32_16x16x32_f16 v[58:61], v[198:201], v[190:193], v[58:61]
	v_mfma_f32_16x16x32_f16 v[54:57], v[206:209], v[182:185], v[54:57]
	v_mfma_f32_16x16x32_f16 v[50:53], v[206:209], v[190:193], v[50:53]
	v_mfma_f32_16x16x32_f16 v[46:49], v[214:217], v[182:185], v[46:49]
	v_mfma_f32_16x16x32_f16 v[42:45], v[214:217], v[190:193], v[42:45]
	v_mfma_f32_16x16x32_f16 v[38:41], v[222:225], v[182:185], v[38:41]
	v_mfma_f32_16x16x32_f16 v[34:37], v[222:225], v[190:193], v[34:37]
	v_mfma_f32_16x16x32_f16 v[62:65], v[202:205], v[186:189], v[62:65]
	v_mfma_f32_16x16x32_f16 v[58:61], v[202:205], v[194:197], v[58:61]
	v_mfma_f32_16x16x32_f16 v[54:57], v[210:213], v[186:189], v[54:57]
	v_mfma_f32_16x16x32_f16 v[50:53], v[210:213], v[194:197], v[50:53]
	v_mfma_f32_16x16x32_f16 v[46:49], v[218:221], v[186:189], v[46:49]
	v_mfma_f32_16x16x32_f16 v[42:45], v[218:221], v[194:197], v[42:45]
	v_mfma_f32_16x16x32_f16 v[38:41], v[226:229], v[186:189], v[38:41]
	v_mfma_f32_16x16x32_f16 v[34:37], v[226:229], v[194:197], v[34:37]
	s_barrier
	s_mov_b32 m0, s84
	v_lshl_add_u64 v[182:183], v[250:251], 0, s[38:39]
	global_load_lds_dwordx4 v[182:183], off
	s_mov_b32 m0, s85
	v_lshl_add_u64 v[182:183], v[252:253], 0, s[38:39]
	global_load_lds_dwordx4 v[182:183], off
	s_waitcnt vmcnt(6)
	s_barrier
	v_mfma_f32_16x16x32_f16 v[30:33], v[198:201], v[230:233], v[30:33]
	v_mfma_f32_16x16x32_f16 v[26:29], v[198:201], v[238:241], v[26:29]
	v_mfma_f32_16x16x32_f16 v[22:25], v[206:209], v[230:233], v[22:25]
	v_mfma_f32_16x16x32_f16 v[18:21], v[206:209], v[238:241], v[18:21]
	v_mfma_f32_16x16x32_f16 v[14:17], v[214:217], v[230:233], v[14:17]
	v_mfma_f32_16x16x32_f16 v[10:13], v[214:217], v[238:241], v[10:13]
	v_mfma_f32_16x16x32_f16 v[6:9], v[222:225], v[230:233], v[6:9]
	v_mfma_f32_16x16x32_f16 v[2:5], v[222:225], v[238:241], v[2:5]
	v_mfma_f32_16x16x32_f16 v[30:33], v[202:205], v[234:237], v[30:33]
	v_mfma_f32_16x16x32_f16 v[26:29], v[202:205], v[242:245], v[26:29]
	v_mfma_f32_16x16x32_f16 v[22:25], v[210:213], v[234:237], v[22:25]
	v_mfma_f32_16x16x32_f16 v[18:21], v[210:213], v[242:245], v[18:21]
	v_mfma_f32_16x16x32_f16 v[14:17], v[218:221], v[234:237], v[14:17]
	v_mfma_f32_16x16x32_f16 v[10:13], v[218:221], v[242:245], v[10:13]
	v_mfma_f32_16x16x32_f16 v[6:9], v[226:229], v[234:237], v[6:9]
	v_mfma_f32_16x16x32_f16 v[2:5], v[226:229], v[242:245], v[2:5]
	s_add_i32 s46, s46, 2
	s_add_u32 s44, s44, 0x100
	s_addc_u32 s45, s45, 0
	s_cmp_lt_u32 s46, 28
	s_barrier
	s_cbranch_scc1 .LBB10_12
	s_add_u32 s42, s42, 0x80f80
	s_addc_u32 s43, s43, 0
	v_readfirstlane_b32 s44, v177
	v_lshl_add_u64 v[130:131], v[130:131], 1, s[42:43]
	s_mov_b32 m0, s44
	ds_read_b128 v[134:137], v171
	ds_read_b128 v[138:141], v173
	ds_read_b128 v[154:157], v174
	ds_read_b128 v[168:171], v175
	ds_read_b128 v[182:185], v176
	ds_read_b128 v[186:189], v176 offset:1024
	ds_read_b128 v[190:193], v176 offset:2048
	ds_read_b128 v[194:197], v176 offset:3072
	ds_read_b128 v[198:201], v176 offset:4096
	ds_read_b128 v[202:205], v176 offset:5120
	ds_read_b128 v[206:209], v176 offset:6144
	ds_read_b128 v[210:213], v176 offset:7168
	global_load_lds_dwordx4 v[130:131], off
	v_lshl_add_u64 v[130:131], v[132:133], 1, s[42:43]
	v_readfirstlane_b32 s42, v178
	s_mov_b32 m0, s42
	s_nop 0
	global_load_lds_dwordx4 v[130:131], off
	s_barrier
	s_waitcnt lgkmcnt(0)
	v_mfma_f32_16x16x32_f16 v[122:125], v[182:185], v[154:157], v[122:125]
	v_mfma_f32_16x16x32_f16 v[110:113], v[198:201], v[134:137], v[110:113]
	v_mfma_f32_16x16x32_f16 v[98:101], v[206:209], v[154:157], v[98:101]
	v_mfma_f32_16x16x32_f16 v[126:129], v[182:185], v[134:137], v[126:129]
	v_mfma_f32_16x16x32_f16 v[122:125], v[186:189], v[168:171], v[122:125]
	v_mfma_f32_16x16x32_f16 v[118:121], v[190:193], v[134:137], v[118:121]
	v_mfma_f32_16x16x32_f16 v[114:117], v[190:193], v[154:157], v[114:117]
	v_mfma_f32_16x16x32_f16 v[130:133], v[202:205], v[138:141], v[110:113]
	v_mfma_f32_16x16x32_f16 v[106:109], v[198:201], v[154:157], v[106:109]
	v_mfma_f32_16x16x32_f16 v[102:105], v[206:209], v[134:137], v[102:105]
	v_mfma_f32_16x16x32_f16 v[98:101], v[210:213], v[168:171], v[98:101]
	v_mfma_f32_16x16x32_f16 v[126:129], v[186:189], v[138:141], v[126:129]
	v_mfma_f32_16x16x32_f16 v[118:121], v[194:197], v[138:141], v[118:121]
	v_mfma_f32_16x16x32_f16 v[114:117], v[194:197], v[168:171], v[114:117]
	v_mfma_f32_16x16x32_f16 v[214:217], v[202:205], v[168:171], v[106:109]
	v_mfma_f32_16x16x32_f16 v[102:105], v[210:213], v[138:141], v[102:105]
	s_barrier
	ds_read_b128 v[106:109], v162
	ds_read_b128 v[110:113], v163
	ds_read_b128 v[160:163], v164
	ds_read_b128 v[218:221], v165
	s_barrier
	s_waitcnt lgkmcnt(0)
	v_mfma_f32_16x16x32_f16 v[82:85], v[190:193], v[160:163], v[82:85]
	v_mfma_f32_16x16x32_f16 v[78:81], v[198:201], v[106:109], v[78:81]
	v_mfma_f32_16x16x32_f16 v[74:77], v[198:201], v[160:163], v[74:77]
	v_mfma_f32_16x16x32_f16 v[70:73], v[206:209], v[106:109], v[70:73]
	v_mfma_f32_16x16x32_f16 v[66:69], v[206:209], v[160:163], v[66:69]
	v_mfma_f32_16x16x32_f16 v[94:97], v[182:185], v[106:109], v[94:97]
	v_mfma_f32_16x16x32_f16 v[90:93], v[182:185], v[160:163], v[90:93]
	v_mfma_f32_16x16x32_f16 v[86:89], v[190:193], v[106:109], v[86:89]
	v_mfma_f32_16x16x32_f16 v[82:85], v[194:197], v[218:221], v[82:85]
	v_mfma_f32_16x16x32_f16 v[78:81], v[202:205], v[110:113], v[78:81]
	v_mfma_f32_16x16x32_f16 v[74:77], v[202:205], v[218:221], v[74:77]
	v_mfma_f32_16x16x32_f16 v[70:73], v[210:213], v[110:113], v[70:73]
	v_mfma_f32_16x16x32_f16 v[66:69], v[210:213], v[218:221], v[66:69]
	v_mfma_f32_16x16x32_f16 v[222:225], v[186:189], v[110:113], v[94:97]
	v_mfma_f32_16x16x32_f16 v[182:185], v[186:189], v[218:221], v[90:93]
	v_mfma_f32_16x16x32_f16 v[86:89], v[194:197], v[110:113], v[86:89]
	s_barrier
	ds_read_b128 v[90:93], v176 offset:16384
	ds_read_b128 v[94:97], v176 offset:17408
	ds_read_b128 v[186:189], v176 offset:18432
	ds_read_b128 v[190:193], v176 offset:19456
	ds_read_b128 v[194:197], v176 offset:20480
	ds_read_b128 v[198:201], v176 offset:21504
	ds_read_b128 v[202:205], v176 offset:22528
	ds_read_b128 v[206:209], v176 offset:23552
	s_waitcnt vmcnt(4)
	s_barrier
	s_waitcnt lgkmcnt(0)
	v_mfma_f32_16x16x32_f16 v[46:49], v[194:197], v[134:137], v[46:49]
	v_mfma_f32_16x16x32_f16 v[42:45], v[194:197], v[154:157], v[42:45]
	v_mfma_f32_16x16x32_f16 v[38:41], v[202:205], v[134:137], v[38:41]
	v_mfma_f32_16x16x32_f16 v[34:37], v[202:205], v[154:157], v[34:37]
	v_mfma_f32_16x16x32_f16 v[62:65], v[90:93], v[134:137], v[62:65]
	v_mfma_f32_16x16x32_f16 v[58:61], v[90:93], v[154:157], v[58:61]
	v_mfma_f32_16x16x32_f16 v[54:57], v[186:189], v[134:137], v[54:57]
	v_mfma_f32_16x16x32_f16 v[50:53], v[186:189], v[154:157], v[50:53]
	v_mfma_f32_16x16x32_f16 v[46:49], v[198:201], v[138:141], v[46:49]
	v_mfma_f32_16x16x32_f16 v[42:45], v[198:201], v[168:171], v[42:45]
	v_mfma_f32_16x16x32_f16 v[38:41], v[206:209], v[138:141], v[38:41]
	v_mfma_f32_16x16x32_f16 v[34:37], v[206:209], v[168:171], v[34:37]
	v_mfma_f32_16x16x32_f16 v[210:213], v[94:97], v[138:141], v[62:65]
	v_mfma_f32_16x16x32_f16 v[226:229], v[94:97], v[168:171], v[58:61]
	v_mfma_f32_16x16x32_f16 v[230:233], v[190:193], v[138:141], v[54:57]
	v_mfma_f32_16x16x32_f16 v[234:237], v[190:193], v[168:171], v[50:53]
	v_mfma_f32_16x16x32_f16 v[2:5], v[202:205], v[160:163], v[2:5]
	v_mfma_f32_16x16x32_f16 v[30:33], v[90:93], v[106:109], v[30:33]
	v_mfma_f32_16x16x32_f16 v[26:29], v[90:93], v[160:163], v[26:29]
	v_mfma_f32_16x16x32_f16 v[22:25], v[186:189], v[106:109], v[22:25]
	v_mfma_f32_16x16x32_f16 v[18:21], v[186:189], v[160:163], v[18:21]
	v_mfma_f32_16x16x32_f16 v[14:17], v[194:197], v[106:109], v[14:17]
	v_mfma_f32_16x16x32_f16 v[10:13], v[194:197], v[160:163], v[10:13]
	v_mfma_f32_16x16x32_f16 v[6:9], v[202:205], v[106:109], v[6:9]
	v_mfma_f32_16x16x32_f16 v[2:5], v[206:209], v[218:221], v[2:5]
	v_mfma_f32_16x16x32_f16 v[138:141], v[94:97], v[110:113], v[30:33]
	v_mfma_f32_16x16x32_f16 v[168:171], v[94:97], v[218:221], v[26:29]
	v_mfma_f32_16x16x32_f16 v[238:241], v[190:193], v[110:113], v[22:25]
	v_mfma_f32_16x16x32_f16 v[186:189], v[190:193], v[218:221], v[18:21]
	v_mfma_f32_16x16x32_f16 v[190:193], v[198:201], v[110:113], v[14:17]
	v_mfma_f32_16x16x32_f16 v[194:197], v[198:201], v[218:221], v[10:13]
	v_mfma_f32_16x16x32_f16 v[198:201], v[206:209], v[110:113], v[6:9]
	s_barrier
	s_nop 0
	ds_read_b128 v[6:9], v144
	ds_read_b128 v[10:13], v145
	ds_read_b128 v[14:17], v146
	ds_read_b128 v[160:163], v147
	ds_read_b128 v[18:21], v176 offset:32768
	ds_read_b128 v[22:25], v176 offset:33792
	ds_read_b128 v[26:29], v176 offset:34816
	ds_read_b128 v[50:53], v176 offset:35840
	ds_read_b128 v[202:205], v176 offset:36864
	ds_read_b128 v[206:209], v176 offset:37888
	ds_read_b128 v[218:221], v176 offset:38912
	ds_read_b128 v[242:245], v176 offset:39936
	s_waitcnt vmcnt(2)
	s_barrier
	s_waitcnt lgkmcnt(0)
	v_mfma_f32_16x16x32_f16 v[30:33], v[18:21], v[6:9], v[126:129]
	v_mfma_f32_16x16x32_f16 v[154:157], v[22:25], v[10:13], v[30:33]
	v_mfma_f32_16x16x32_f16 v[30:33], v[18:21], v[14:17], v[122:125]
	v_mfma_f32_16x16x32_f16 v[110:113], v[22:25], v[160:163], v[30:33]
	v_mfma_f32_16x16x32_f16 v[30:33], v[26:29], v[6:9], v[118:121]
	v_mfma_f32_16x16x32_f16 v[146:149], v[50:53], v[10:13], v[30:33]
	v_mfma_f32_16x16x32_f16 v[30:33], v[26:29], v[14:17], v[114:117]
	v_mfma_f32_16x16x32_f16 v[106:109], v[50:53], v[160:163], v[30:33]
	v_mfma_f32_16x16x32_f16 v[30:33], v[202:205], v[6:9], v[130:133]
	v_mfma_f32_16x16x32_f16 v[142:145], v[206:209], v[10:13], v[30:33]
	v_mfma_f32_16x16x32_f16 v[30:33], v[202:205], v[14:17], v[214:217]
	v_mfma_f32_16x16x32_f16 v[94:97], v[206:209], v[160:163], v[30:33]
	v_mfma_f32_16x16x32_f16 v[30:33], v[218:221], v[6:9], v[102:105]
	v_mfma_f32_16x16x32_f16 v[134:137], v[242:245], v[10:13], v[30:33]
	v_mfma_f32_16x16x32_f16 v[30:33], v[218:221], v[14:17], v[98:101]
	v_mfma_f32_16x16x32_f16 v[90:93], v[242:245], v[160:163], v[30:33]
	s_barrier
	ds_read_b128 v[102:105], v150
	ds_read_b128 v[114:117], v151
	ds_read_b128 v[118:121], v152
	ds_read_b128 v[126:129], v153
	s_waitcnt vmcnt(0)
	s_barrier
	s_waitcnt lgkmcnt(0)
	v_mfma_f32_16x16x32_f16 v[30:33], v[18:21], v[102:105], v[222:225]
	v_mfma_f32_16x16x32_f16 v[18:21], v[18:21], v[118:121], v[182:185]
	v_mfma_f32_16x16x32_f16 v[62:65], v[22:25], v[114:117], v[30:33]
	v_mfma_f32_16x16x32_f16 v[30:33], v[22:25], v[126:129], v[18:21]
	v_mfma_f32_16x16x32_f16 v[18:21], v[26:29], v[102:105], v[86:89]
	v_mfma_f32_16x16x32_f16 v[58:61], v[50:53], v[114:117], v[18:21]
	v_mfma_f32_16x16x32_f16 v[18:21], v[26:29], v[118:121], v[82:85]
	v_mfma_f32_16x16x32_f16 v[26:29], v[50:53], v[126:129], v[18:21]
	v_mfma_f32_16x16x32_f16 v[18:21], v[202:205], v[102:105], v[78:81]
	v_mfma_f32_16x16x32_f16 v[54:57], v[206:209], v[114:117], v[18:21]
	v_mfma_f32_16x16x32_f16 v[18:21], v[202:205], v[118:121], v[74:77]
	v_mfma_f32_16x16x32_f16 v[22:25], v[206:209], v[126:129], v[18:21]
	v_mfma_f32_16x16x32_f16 v[18:21], v[218:221], v[102:105], v[70:73]
	v_mfma_f32_16x16x32_f16 v[50:53], v[242:245], v[114:117], v[18:21]
	v_mfma_f32_16x16x32_f16 v[18:21], v[218:221], v[118:121], v[66:69]
	v_mfma_f32_16x16x32_f16 v[18:21], v[242:245], v[126:129], v[18:21]
	s_barrier
	ds_read_b128 v[86:89], v176 offset:49152
	ds_read_b128 v[150:153], v176 offset:50176
	ds_read_b128 v[182:185], v176 offset:51200
	ds_read_b128 v[202:205], v176 offset:52224
	ds_read_b128 v[206:209], v176 offset:53248
	ds_read_b128 v[214:217], v176 offset:54272
	ds_read_b128 v[218:221], v176 offset:55296
	ds_read_b128 v[174:177], v176 offset:56320
	s_barrier
	s_waitcnt lgkmcnt(0)
	v_mfma_f32_16x16x32_f16 v[66:69], v[86:89], v[6:9], v[210:213]
	v_mfma_f32_16x16x32_f16 v[130:133], v[150:153], v[10:13], v[66:69]
	v_mfma_f32_16x16x32_f16 v[66:69], v[86:89], v[14:17], v[226:229]
	v_mfma_f32_16x16x32_f16 v[78:81], v[150:153], v[160:163], v[66:69]
	v_mfma_f32_16x16x32_f16 v[66:69], v[182:185], v[6:9], v[230:233]
	v_mfma_f32_16x16x32_f16 v[46:49], v[206:209], v[6:9], v[46:49]
	v_mfma_f32_16x16x32_f16 v[6:9], v[218:221], v[6:9], v[38:41]
	v_mfma_f32_16x16x32_f16 v[122:125], v[202:205], v[10:13], v[66:69]
	v_mfma_f32_16x16x32_f16 v[66:69], v[182:185], v[14:17], v[234:237]
	v_mfma_f32_16x16x32_f16 v[42:45], v[206:209], v[14:17], v[42:45]
	v_mfma_f32_16x16x32_f16 v[82:85], v[174:177], v[10:13], v[6:9]
	v_mfma_f32_16x16x32_f16 v[6:9], v[218:221], v[14:17], v[34:37]
	v_mfma_f32_16x16x32_f16 v[74:77], v[202:205], v[160:163], v[66:69]
	v_mfma_f32_16x16x32_f16 v[98:101], v[214:217], v[10:13], v[46:49]
	v_mfma_f32_16x16x32_f16 v[70:73], v[214:217], v[160:163], v[42:45]
	v_mfma_f32_16x16x32_f16 v[66:69], v[174:177], v[160:163], v[6:9]
	v_mfma_f32_16x16x32_f16 v[6:9], v[86:89], v[102:105], v[138:141]
	v_mfma_f32_16x16x32_f16 v[46:49], v[150:153], v[114:117], v[6:9]
	v_mfma_f32_16x16x32_f16 v[6:9], v[86:89], v[118:121], v[168:171]
	v_mfma_f32_16x16x32_f16 v[14:17], v[150:153], v[126:129], v[6:9]
	v_mfma_f32_16x16x32_f16 v[6:9], v[182:185], v[102:105], v[238:241]
	v_mfma_f32_16x16x32_f16 v[42:45], v[202:205], v[114:117], v[6:9]
	v_mfma_f32_16x16x32_f16 v[6:9], v[182:185], v[118:121], v[186:189]
	v_mfma_f32_16x16x32_f16 v[10:13], v[202:205], v[126:129], v[6:9]
	v_mfma_f32_16x16x32_f16 v[6:9], v[206:209], v[102:105], v[190:193]
	v_mfma_f32_16x16x32_f16 v[38:41], v[214:217], v[114:117], v[6:9]
	v_mfma_f32_16x16x32_f16 v[6:9], v[206:209], v[118:121], v[194:197]
	v_mfma_f32_16x16x32_f16 v[34:37], v[218:221], v[102:105], v[198:201]
	v_mfma_f32_16x16x32_f16 v[2:5], v[218:221], v[118:121], v[2:5]
	v_mfma_f32_16x16x32_f16 v[6:9], v[214:217], v[126:129], v[6:9]
	v_mfma_f32_16x16x32_f16 v[34:37], v[174:177], v[114:117], v[34:37]
	v_mfma_f32_16x16x32_f16 v[2:5], v[174:177], v[126:129], v[2:5]
	s_cmpk_gt_u32 s61, 0xff
	s_barrier
	s_cbranch_scc1 .LBB10_15
	s_barrier
